# P2 pipelined + write-through (sc1) stores in the four GEMM epilogues so the grid barrier's L2 write-back has less to flush
# baseline (speedup 1.0000x reference)
.LBB0_124:
	v_lshl_or_b32 v170, s6, 8, v173
	v_mov_b64_e32 v[114:115], s[8:9]
	v_ashrrev_i32_e32 v171, 31, v170
	v_mad_i64_i32 v[114:115], s[6:7], v168, s43, v[114:115]
	v_lshl_add_u64 v[118:119], v[170:171], 1, v[114:115]
	v_cvt_pk_bf16_f32 v114, v130, v131
	v_cvt_pk_bf16_f32 v115, v132, v133
	v_cvt_pk_bf16_f32 v116, v134, v135
	v_cvt_pk_bf16_f32 v117, v136, v137
	global_store_dwordx4 v[118:119], v[114:117], off sc1
	s_andn2_b64 vcc, exec, s[26:27]
	s_mov_b64 s[24:25], -1
	v_cvt_pk_bf16_f32 v114, v138, v139
	v_cvt_pk_bf16_f32 v115, v140, v141
	v_cvt_pk_bf16_f32 v116, v142, v143
	v_cvt_pk_bf16_f32 v117, v144, v145
	global_store_dwordx4 v[118:119], v[114:117], off offset:256 sc1
	s_nop 1
	v_cndmask_b32_e64 v114, 0, 1, s[26:27]
	v_cmp_ne_u32_e64 s[6:7], 1, v114
	s_cbranch_vccnz .LBB0_132
	s_andn2_b64 vcc, exec, s[22:23]
	s_cbranch_vccnz .LBB0_129
	v_mov_b64_e32 v[116:117], v[112:113]
	v_mov_b64_e32 v[120:121], v[108:109]
	v_mov_b64_e32 v[124:125], v[104:105]
	v_mov_b64_e32 v[128:129], v[100:101]
	s_andn2_b64 vcc, exec, s[20:21]
	v_mov_b64_e32 v[114:115], v[110:111]
	v_mov_b64_e32 v[118:119], v[106:107]
	v_mov_b64_e32 v[122:123], v[102:103]
	v_mov_b64_e32 v[126:127], v[98:99]
	s_cbranch_vccnz .LBB0_128
	v_mul_f32_e32 v115, 0x3d372713, v106
	v_mul_f32_e32 v115, v106, v115
	v_mul_f32_e32 v116, 0x3d372713, v102
	v_fma_f32 v115, v106, v115, v106
	v_mul_f32_e32 v116, v102, v116
	v_mul_f32_e32 v117, 0x3d372713, v98
	v_mul_f32_e32 v115, 0x3fcc422a, v115
	v_fma_f32 v116, v102, v116, v102
	v_mul_f32_e32 v117, v98, v117
	v_mul_f32_e32 v115, 0xbfb8aa3b, v115
	v_mul_f32_e32 v116, 0x3fcc422a, v116
	v_fma_f32 v117, v98, v117, v98
	v_exp_f32_e32 v115, v115
	v_mul_f32_e32 v116, 0xbfb8aa3b, v116
	v_mul_f32_e32 v117, 0x3fcc422a, v117
	v_exp_f32_e32 v116, v116
	v_mul_f32_e32 v117, 0xbfb8aa3b, v117
	v_exp_f32_e32 v117, v117
	v_add_f32_e32 v115, 1.0, v115
	v_rcp_f32_e32 v118, v115
	v_add_f32_e32 v115, 1.0, v116
	v_rcp_f32_e32 v122, v115
	v_add_f32_e32 v115, 1.0, v117
	v_mul_f32_e32 v116, 0x3d372713, v111
	v_mul_f32_e32 v117, 0x3d372713, v107
	v_mul_f32_e32 v116, v111, v116
	v_mul_f32_e32 v117, v107, v117
	v_fma_f32 v116, v111, v116, v111
	v_fma_f32 v117, v107, v117, v107
	v_mul_f32_e32 v116, 0x3fcc422a, v116
	v_mul_f32_e32 v117, 0x3fcc422a, v117
	v_mul_f32_e32 v116, 0xbfb8aa3b, v116
	v_mul_f32_e32 v117, 0xbfb8aa3b, v117
	v_exp_f32_e32 v116, v116
	v_exp_f32_e32 v117, v117
	v_rcp_f32_e32 v126, v115
	v_mul_f32_e32 v119, 0x3d372713, v99
	v_add_f32_e32 v115, 1.0, v116
	v_add_f32_e32 v116, 1.0, v117
	v_mul_f32_e32 v117, 0x3d372713, v103
	v_mul_f32_e32 v117, v103, v117
	v_fma_f32 v117, v103, v117, v103
	v_mul_f32_e32 v119, v99, v119
	v_mul_f32_e32 v117, 0x3fcc422a, v117
	v_fma_f32 v119, v99, v119, v99
	v_mul_f32_e32 v117, 0xbfb8aa3b, v117
	v_mul_f32_e32 v119, 0x3fcc422a, v119
	v_exp_f32_e32 v117, v117
	v_mul_f32_e32 v119, 0xbfb8aa3b, v119
	v_exp_f32_e32 v120, v119
	v_rcp_f32_e32 v119, v116
	v_add_f32_e32 v116, 1.0, v117
	v_rcp_f32_e32 v123, v116
	v_add_f32_e32 v116, 1.0, v120
	v_mul_f32_e32 v117, 0x3d372713, v112
	v_mul_f32_e32 v120, 0x3d372713, v108
	v_mul_f32_e32 v117, v112, v117
	v_mul_f32_e32 v120, v108, v120
	v_fma_f32 v117, v112, v117, v112
	v_fma_f32 v120, v108, v120, v108
	v_mul_f32_e32 v117, 0x3fcc422a, v117
	v_mul_f32_e32 v120, 0x3fcc422a, v120
	v_mul_f32_e32 v117, 0xbfb8aa3b, v117
	v_mul_f32_e32 v120, 0xbfb8aa3b, v120
	v_exp_f32_e32 v117, v117
	v_exp_f32_e32 v120, v120
	v_rcp_f32_e32 v127, v116
	v_mul_f32_e32 v124, 0x3d372713, v113
	v_add_f32_e32 v116, 1.0, v117
	v_add_f32_e32 v117, 1.0, v120
	v_rcp_f32_e32 v120, v117
	v_mul_f32_e32 v117, 0x3d372713, v104
	v_mul_f32_e32 v117, v104, v117
	v_fma_f32 v117, v104, v117, v104
	v_mul_f32_e32 v124, v113, v124
	v_mul_f32_e32 v117, 0x3fcc422a, v117
	v_fma_f32 v124, v113, v124, v113
	v_mul_f32_e32 v117, 0xbfb8aa3b, v117
	v_mul_f32_e32 v124, 0x3fcc422a, v124
	v_exp_f32_e32 v117, v117
	v_mul_f32_e32 v124, 0xbfb8aa3b, v124
	v_exp_f32_e32 v125, v124
	v_mul_f32_e32 v121, 0x3d372713, v100
	v_add_f32_e32 v117, 1.0, v117
	v_mul_f32_e32 v121, v100, v121
	v_rcp_f32_e32 v124, v117
	v_add_f32_e32 v117, 1.0, v125
	v_mul_f32_e32 v125, 0x3d372713, v109
	v_fma_f32 v121, v100, v121, v100
	v_mul_f32_e32 v125, v109, v125
	v_mul_f32_e32 v121, 0x3fcc422a, v121
	v_fma_f32 v125, v109, v125, v109
	v_mul_f32_e32 v121, 0xbfb8aa3b, v121
	v_mul_f32_e32 v125, 0x3fcc422a, v125
	v_exp_f32_e32 v121, v121
	v_mul_f32_e32 v125, 0xbfb8aa3b, v125
	v_exp_f32_e32 v125, v125
	v_mul_f32_e32 v114, 0x3d372713, v110
	v_add_f32_e32 v121, 1.0, v121
	v_rcp_f32_e32 v128, v121
	v_add_f32_e32 v121, 1.0, v125
	v_mul_f32_e32 v125, 0x3d372713, v105
	v_mul_f32_e32 v129, 0x3d372713, v101
	v_mul_f32_e32 v114, v110, v114
	v_mul_f32_e32 v125, v105, v125
	v_mul_f32_e32 v129, v101, v129
	v_fma_f32 v114, v110, v114, v110
	v_fma_f32 v125, v105, v125, v105
	v_fma_f32 v129, v101, v129, v101
	v_mul_f32_e32 v114, 0x3fcc422a, v114
	v_mul_f32_e32 v125, 0x3fcc422a, v125
	v_mul_f32_e32 v129, 0x3fcc422a, v129
	v_mul_f32_e32 v114, 0xbfb8aa3b, v114
	v_mul_f32_e32 v125, 0xbfb8aa3b, v125
	v_mul_f32_e32 v129, 0xbfb8aa3b, v129
	v_exp_f32_e32 v114, v114
	v_exp_f32_e32 v125, v125
	v_exp_f32_e32 v129, v129
	v_rcp_f32_e32 v115, v115
	v_add_f32_e32 v114, 1.0, v114
	v_add_f32_e32 v125, 1.0, v125
	v_add_f32_e32 v129, 1.0, v129
	v_rcp_f32_e32 v114, v114
	v_rcp_f32_e32 v116, v116
	v_rcp_f32_e32 v117, v117
	v_rcp_f32_e32 v121, v121
	v_rcp_f32_e32 v125, v125
	v_rcp_f32_e32 v129, v129
	v_pk_mul_f32 v[116:117], v[112:113], v[116:117]
	v_pk_mul_f32 v[114:115], v[110:111], v[114:115]
	v_pk_mul_f32 v[120:121], v[108:109], v[120:121]
	v_pk_mul_f32 v[118:119], v[106:107], v[118:119]
	v_pk_mul_f32 v[124:125], v[104:105], v[124:125]
	v_pk_mul_f32 v[122:123], v[102:103], v[122:123]
	v_pk_mul_f32 v[128:129], v[100:101], v[128:129]
	v_pk_mul_f32 v[126:127], v[98:99], v[126:127]

.LBB0_134:
	v_mov_b64_e32 v[98:99], s[8:9]
	v_mad_i64_i32 v[98:99], s[24:25], v130, s43, v[98:99]
	v_lshl_add_u64 v[102:103], v[170:171], 1, v[98:99]
	v_cvt_pk_bf16_f32 v98, v114, v115
	v_cvt_pk_bf16_f32 v99, v116, v117
	v_cvt_pk_bf16_f32 v100, v118, v119
	v_cvt_pk_bf16_f32 v101, v120, v121
	global_store_dwordx4 v[102:103], v[98:101], off sc1
	s_and_b64 vcc, exec, s[6:7]
	s_mov_b64 s[24:25], -1
	v_cvt_pk_bf16_f32 v98, v122, v123
	v_cvt_pk_bf16_f32 v99, v124, v125
	v_cvt_pk_bf16_f32 v100, v126, v127
	v_cvt_pk_bf16_f32 v101, v128, v129
	global_store_dwordx4 v[102:103], v[98:101], off offset:256 sc1
	s_cbranch_vccnz .LBB0_142
	s_andn2_b64 vcc, exec, s[22:23]
	s_cbranch_vccnz .LBB0_139
	v_mov_b64_e32 v[100:101], v[96:97]
	v_mov_b64_e32 v[104:105], v[92:93]
	v_mov_b64_e32 v[108:109], v[88:89]
	v_mov_b64_e32 v[112:113], v[84:85]
	s_andn2_b64 vcc, exec, s[20:21]
	v_mov_b64_e32 v[98:99], v[94:95]
	v_mov_b64_e32 v[102:103], v[90:91]
	v_mov_b64_e32 v[106:107], v[86:87]
	v_mov_b64_e32 v[110:111], v[82:83]
	s_cbranch_vccnz .LBB0_138
	v_mul_f32_e32 v99, 0x3d372713, v90
	v_mul_f32_e32 v99, v90, v99
	v_mul_f32_e32 v100, 0x3d372713, v86
	v_fma_f32 v99, v90, v99, v90
	v_mul_f32_e32 v100, v86, v100
	v_mul_f32_e32 v101, 0x3d372713, v82
	v_mul_f32_e32 v99, 0x3fcc422a, v99
	v_fma_f32 v100, v86, v100, v86
	v_mul_f32_e32 v101, v82, v101
	v_mul_f32_e32 v99, 0xbfb8aa3b, v99
	v_mul_f32_e32 v100, 0x3fcc422a, v100
	v_fma_f32 v101, v82, v101, v82
	v_exp_f32_e32 v99, v99
	v_mul_f32_e32 v100, 0xbfb8aa3b, v100
	v_mul_f32_e32 v101, 0x3fcc422a, v101
	v_exp_f32_e32 v100, v100
	v_mul_f32_e32 v101, 0xbfb8aa3b, v101
	v_exp_f32_e32 v101, v101
	v_add_f32_e32 v99, 1.0, v99
	v_rcp_f32_e32 v102, v99
	v_add_f32_e32 v99, 1.0, v100
	v_rcp_f32_e32 v106, v99
	v_add_f32_e32 v99, 1.0, v101
	v_mul_f32_e32 v100, 0x3d372713, v95
	v_mul_f32_e32 v101, 0x3d372713, v91
	v_mul_f32_e32 v100, v95, v100
	v_mul_f32_e32 v101, v91, v101
	v_fma_f32 v100, v95, v100, v95
	v_fma_f32 v101, v91, v101, v91
	v_mul_f32_e32 v100, 0x3fcc422a, v100
	v_mul_f32_e32 v101, 0x3fcc422a, v101
	v_mul_f32_e32 v100, 0xbfb8aa3b, v100
	v_mul_f32_e32 v101, 0xbfb8aa3b, v101
	v_exp_f32_e32 v100, v100
	v_exp_f32_e32 v101, v101
	v_rcp_f32_e32 v110, v99
	v_mul_f32_e32 v103, 0x3d372713, v83
	v_add_f32_e32 v99, 1.0, v100
	v_add_f32_e32 v100, 1.0, v101
	v_mul_f32_e32 v101, 0x3d372713, v87
	v_mul_f32_e32 v101, v87, v101
	v_fma_f32 v101, v87, v101, v87
	v_mul_f32_e32 v103, v83, v103
	v_mul_f32_e32 v101, 0x3fcc422a, v101
	v_fma_f32 v103, v83, v103, v83
	v_mul_f32_e32 v101, 0xbfb8aa3b, v101
	v_mul_f32_e32 v103, 0x3fcc422a, v103
	v_exp_f32_e32 v101, v101
	v_mul_f32_e32 v103, 0xbfb8aa3b, v103
	v_exp_f32_e32 v104, v103
	v_rcp_f32_e32 v103, v100
	v_add_f32_e32 v100, 1.0, v101
	v_rcp_f32_e32 v107, v100
	v_add_f32_e32 v100, 1.0, v104
	v_mul_f32_e32 v101, 0x3d372713, v96
	v_mul_f32_e32 v104, 0x3d372713, v92
	v_mul_f32_e32 v101, v96, v101
	v_mul_f32_e32 v104, v92, v104
	v_fma_f32 v101, v96, v101, v96
	v_fma_f32 v104, v92, v104, v92
	v_mul_f32_e32 v101, 0x3fcc422a, v101
	v_mul_f32_e32 v104, 0x3fcc422a, v104
	v_mul_f32_e32 v101, 0xbfb8aa3b, v101
	v_mul_f32_e32 v104, 0xbfb8aa3b, v104
	v_exp_f32_e32 v101, v101
	v_exp_f32_e32 v104, v104
	v_rcp_f32_e32 v111, v100
	v_mul_f32_e32 v108, 0x3d372713, v97
	v_add_f32_e32 v100, 1.0, v101
	v_add_f32_e32 v101, 1.0, v104
	v_rcp_f32_e32 v104, v101
	v_mul_f32_e32 v101, 0x3d372713, v88
	v_mul_f32_e32 v101, v88, v101
	v_fma_f32 v101, v88, v101, v88
	v_mul_f32_e32 v108, v97, v108
	v_mul_f32_e32 v101, 0x3fcc422a, v101
	v_fma_f32 v108, v97, v108, v97
	v_mul_f32_e32 v101, 0xbfb8aa3b, v101
	v_mul_f32_e32 v108, 0x3fcc422a, v108
	v_exp_f32_e32 v101, v101
	v_mul_f32_e32 v108, 0xbfb8aa3b, v108
	v_exp_f32_e32 v109, v108
	v_mul_f32_e32 v105, 0x3d372713, v84
	v_add_f32_e32 v101, 1.0, v101
	v_mul_f32_e32 v105, v84, v105
	v_rcp_f32_e32 v108, v101
	v_add_f32_e32 v101, 1.0, v109
	v_mul_f32_e32 v109, 0x3d372713, v93
	v_fma_f32 v105, v84, v105, v84
	v_mul_f32_e32 v109, v93, v109
	v_mul_f32_e32 v105, 0x3fcc422a, v105
	v_fma_f32 v109, v93, v109, v93
	v_mul_f32_e32 v105, 0xbfb8aa3b, v105
	v_mul_f32_e32 v109, 0x3fcc422a, v109
	v_exp_f32_e32 v105, v105
	v_mul_f32_e32 v109, 0xbfb8aa3b, v109
	v_exp_f32_e32 v109, v109
	v_mul_f32_e32 v98, 0x3d372713, v94
	v_add_f32_e32 v105, 1.0, v105
	v_rcp_f32_e32 v112, v105
	v_add_f32_e32 v105, 1.0, v109
	v_mul_f32_e32 v109, 0x3d372713, v89
	v_mul_f32_e32 v113, 0x3d372713, v85
	v_mul_f32_e32 v98, v94, v98
	v_mul_f32_e32 v109, v89, v109
	v_mul_f32_e32 v113, v85, v113
	v_fma_f32 v98, v94, v98, v94
	v_fma_f32 v109, v89, v109, v89
	v_fma_f32 v113, v85, v113, v85
	v_mul_f32_e32 v98, 0x3fcc422a, v98
	v_mul_f32_e32 v109, 0x3fcc422a, v109
	v_mul_f32_e32 v113, 0x3fcc422a, v113
	v_mul_f32_e32 v98, 0xbfb8aa3b, v98
	v_mul_f32_e32 v109, 0xbfb8aa3b, v109
	v_mul_f32_e32 v113, 0xbfb8aa3b, v113
	v_exp_f32_e32 v98, v98
	v_exp_f32_e32 v109, v109
	v_exp_f32_e32 v113, v113
	v_rcp_f32_e32 v99, v99
	v_add_f32_e32 v98, 1.0, v98
	v_add_f32_e32 v109, 1.0, v109
	v_add_f32_e32 v113, 1.0, v113
	v_rcp_f32_e32 v98, v98
	v_rcp_f32_e32 v100, v100
	v_rcp_f32_e32 v101, v101
	v_rcp_f32_e32 v105, v105
	v_rcp_f32_e32 v109, v109
	v_rcp_f32_e32 v113, v113
	v_pk_mul_f32 v[100:101], v[96:97], v[100:101]
	v_pk_mul_f32 v[98:99], v[94:95], v[98:99]
	v_pk_mul_f32 v[104:105], v[92:93], v[104:105]
	v_pk_mul_f32 v[102:103], v[90:91], v[102:103]
	v_pk_mul_f32 v[108:109], v[88:89], v[108:109]
	v_pk_mul_f32 v[106:107], v[86:87], v[106:107]
	v_pk_mul_f32 v[112:113], v[84:85], v[112:113]
	v_pk_mul_f32 v[110:111], v[82:83], v[110:111]

.LBB0_144:
	v_mov_b64_e32 v[82:83], s[8:9]
	v_mad_i64_i32 v[82:83], s[24:25], v114, s43, v[82:83]
	v_lshl_add_u64 v[86:87], v[170:171], 1, v[82:83]
	v_cvt_pk_bf16_f32 v82, v98, v99
	v_cvt_pk_bf16_f32 v83, v100, v101
	v_cvt_pk_bf16_f32 v84, v102, v103
	v_cvt_pk_bf16_f32 v85, v104, v105
	global_store_dwordx4 v[86:87], v[82:85], off sc1
	s_and_b64 vcc, exec, s[6:7]
	s_mov_b64 s[24:25], -1
	v_cvt_pk_bf16_f32 v82, v106, v107
	v_cvt_pk_bf16_f32 v83, v108, v109
	v_cvt_pk_bf16_f32 v84, v110, v111
	v_cvt_pk_bf16_f32 v85, v112, v113
	global_store_dwordx4 v[86:87], v[82:85], off offset:256 sc1
	s_cbranch_vccnz .LBB0_152
	s_andn2_b64 vcc, exec, s[22:23]
	s_cbranch_vccnz .LBB0_149
	v_mov_b64_e32 v[84:85], v[80:81]
	v_mov_b64_e32 v[88:89], v[76:77]
	v_mov_b64_e32 v[92:93], v[72:73]
	v_mov_b64_e32 v[96:97], v[68:69]
	s_andn2_b64 vcc, exec, s[20:21]
	v_mov_b64_e32 v[82:83], v[78:79]
	v_mov_b64_e32 v[86:87], v[74:75]
	v_mov_b64_e32 v[90:91], v[70:71]
	v_mov_b64_e32 v[94:95], v[66:67]
	s_cbranch_vccnz .LBB0_148
	v_mul_f32_e32 v83, 0x3d372713, v74
	v_mul_f32_e32 v83, v74, v83
	v_mul_f32_e32 v84, 0x3d372713, v70
	v_fma_f32 v83, v74, v83, v74
	v_mul_f32_e32 v84, v70, v84
	v_mul_f32_e32 v85, 0x3d372713, v66
	v_mul_f32_e32 v83, 0x3fcc422a, v83
	v_fma_f32 v84, v70, v84, v70
	v_mul_f32_e32 v85, v66, v85
	v_mul_f32_e32 v83, 0xbfb8aa3b, v83
	v_mul_f32_e32 v84, 0x3fcc422a, v84
	v_fma_f32 v85, v66, v85, v66
	v_exp_f32_e32 v83, v83
	v_mul_f32_e32 v84, 0xbfb8aa3b, v84
	v_mul_f32_e32 v85, 0x3fcc422a, v85
	v_exp_f32_e32 v84, v84
	v_mul_f32_e32 v85, 0xbfb8aa3b, v85
	v_exp_f32_e32 v85, v85
	v_add_f32_e32 v83, 1.0, v83
	v_rcp_f32_e32 v86, v83
	v_add_f32_e32 v83, 1.0, v84
	v_rcp_f32_e32 v90, v83
	v_add_f32_e32 v83, 1.0, v85
	v_mul_f32_e32 v84, 0x3d372713, v79
	v_mul_f32_e32 v85, 0x3d372713, v75
	v_mul_f32_e32 v84, v79, v84
	v_mul_f32_e32 v85, v75, v85
	v_fma_f32 v84, v79, v84, v79
	v_fma_f32 v85, v75, v85, v75
	v_mul_f32_e32 v84, 0x3fcc422a, v84
	v_mul_f32_e32 v85, 0x3fcc422a, v85
	v_mul_f32_e32 v84, 0xbfb8aa3b, v84
	v_mul_f32_e32 v85, 0xbfb8aa3b, v85
	v_exp_f32_e32 v84, v84
	v_exp_f32_e32 v85, v85
	v_rcp_f32_e32 v94, v83
	v_mul_f32_e32 v87, 0x3d372713, v67
	v_add_f32_e32 v83, 1.0, v84
	v_add_f32_e32 v84, 1.0, v85
	v_mul_f32_e32 v85, 0x3d372713, v71
	v_mul_f32_e32 v85, v71, v85
	v_fma_f32 v85, v71, v85, v71
	v_mul_f32_e32 v87, v67, v87
	v_mul_f32_e32 v85, 0x3fcc422a, v85
	v_fma_f32 v87, v67, v87, v67
	v_mul_f32_e32 v85, 0xbfb8aa3b, v85
	v_mul_f32_e32 v87, 0x3fcc422a, v87
	v_exp_f32_e32 v85, v85
	v_mul_f32_e32 v87, 0xbfb8aa3b, v87
	v_exp_f32_e32 v88, v87
	v_rcp_f32_e32 v87, v84
	v_add_f32_e32 v84, 1.0, v85
	v_rcp_f32_e32 v91, v84
	v_add_f32_e32 v84, 1.0, v88
	v_mul_f32_e32 v85, 0x3d372713, v80
	v_mul_f32_e32 v88, 0x3d372713, v76
	v_mul_f32_e32 v85, v80, v85
	v_mul_f32_e32 v88, v76, v88
	v_fma_f32 v85, v80, v85, v80
	v_fma_f32 v88, v76, v88, v76
	v_mul_f32_e32 v85, 0x3fcc422a, v85
	v_mul_f32_e32 v88, 0x3fcc422a, v88
	v_mul_f32_e32 v85, 0xbfb8aa3b, v85
	v_mul_f32_e32 v88, 0xbfb8aa3b, v88
	v_exp_f32_e32 v85, v85
	v_exp_f32_e32 v88, v88
	v_rcp_f32_e32 v95, v84
	v_mul_f32_e32 v92, 0x3d372713, v81
	v_add_f32_e32 v84, 1.0, v85
	v_add_f32_e32 v85, 1.0, v88
	v_rcp_f32_e32 v88, v85
	v_mul_f32_e32 v85, 0x3d372713, v72
	v_mul_f32_e32 v85, v72, v85
	v_fma_f32 v85, v72, v85, v72
	v_mul_f32_e32 v92, v81, v92
	v_mul_f32_e32 v85, 0x3fcc422a, v85
	v_fma_f32 v92, v81, v92, v81
	v_mul_f32_e32 v85, 0xbfb8aa3b, v85
	v_mul_f32_e32 v92, 0x3fcc422a, v92
	v_exp_f32_e32 v85, v85
	v_mul_f32_e32 v92, 0xbfb8aa3b, v92
	v_exp_f32_e32 v93, v92
	v_mul_f32_e32 v89, 0x3d372713, v68
	v_add_f32_e32 v85, 1.0, v85
	v_mul_f32_e32 v89, v68, v89
	v_rcp_f32_e32 v92, v85
	v_add_f32_e32 v85, 1.0, v93
	v_mul_f32_e32 v93, 0x3d372713, v77
	v_fma_f32 v89, v68, v89, v68
	v_mul_f32_e32 v93, v77, v93
	v_mul_f32_e32 v89, 0x3fcc422a, v89
	v_fma_f32 v93, v77, v93, v77
	v_mul_f32_e32 v89, 0xbfb8aa3b, v89
	v_mul_f32_e32 v93, 0x3fcc422a, v93
	v_exp_f32_e32 v89, v89
	v_mul_f32_e32 v93, 0xbfb8aa3b, v93
	v_exp_f32_e32 v93, v93
	v_mul_f32_e32 v82, 0x3d372713, v78
	v_add_f32_e32 v89, 1.0, v89
	v_rcp_f32_e32 v96, v89
	v_add_f32_e32 v89, 1.0, v93
	v_mul_f32_e32 v93, 0x3d372713, v73
	v_mul_f32_e32 v97, 0x3d372713, v69
	v_mul_f32_e32 v82, v78, v82
	v_mul_f32_e32 v93, v73, v93
	v_mul_f32_e32 v97, v69, v97
	v_fma_f32 v82, v78, v82, v78
	v_fma_f32 v93, v73, v93, v73
	v_fma_f32 v97, v69, v97, v69
	v_mul_f32_e32 v82, 0x3fcc422a, v82
	v_mul_f32_e32 v93, 0x3fcc422a, v93
	v_mul_f32_e32 v97, 0x3fcc422a, v97
	v_mul_f32_e32 v82, 0xbfb8aa3b, v82
	v_mul_f32_e32 v93, 0xbfb8aa3b, v93
	v_mul_f32_e32 v97, 0xbfb8aa3b, v97
	v_exp_f32_e32 v82, v82
	v_exp_f32_e32 v93, v93
	v_exp_f32_e32 v97, v97
	v_rcp_f32_e32 v83, v83
	v_add_f32_e32 v82, 1.0, v82
	v_add_f32_e32 v93, 1.0, v93
	v_add_f32_e32 v97, 1.0, v97
	v_rcp_f32_e32 v82, v82
	v_rcp_f32_e32 v84, v84
	v_rcp_f32_e32 v85, v85
	v_rcp_f32_e32 v89, v89
	v_rcp_f32_e32 v93, v93
	v_rcp_f32_e32 v97, v97
	v_pk_mul_f32 v[84:85], v[80:81], v[84:85]
	v_pk_mul_f32 v[82:83], v[78:79], v[82:83]
	v_pk_mul_f32 v[88:89], v[76:77], v[88:89]
	v_pk_mul_f32 v[86:87], v[74:75], v[86:87]
	v_pk_mul_f32 v[92:93], v[72:73], v[92:93]
	v_pk_mul_f32 v[90:91], v[70:71], v[90:91]
	v_pk_mul_f32 v[96:97], v[68:69], v[96:97]
	v_pk_mul_f32 v[94:95], v[66:67], v[94:95]

.LBB0_154:
	v_mov_b64_e32 v[66:67], s[8:9]
	v_mad_i64_i32 v[66:67], s[24:25], v98, s43, v[66:67]
	v_lshl_add_u64 v[70:71], v[170:171], 1, v[66:67]
	v_cvt_pk_bf16_f32 v66, v82, v83
	v_cvt_pk_bf16_f32 v67, v84, v85
	v_cvt_pk_bf16_f32 v68, v86, v87
	v_cvt_pk_bf16_f32 v69, v88, v89
	global_store_dwordx4 v[70:71], v[66:69], off sc1
	s_and_b64 vcc, exec, s[6:7]
	s_mov_b64 s[24:25], -1
	v_cvt_pk_bf16_f32 v66, v90, v91
	v_cvt_pk_bf16_f32 v67, v92, v93
	v_cvt_pk_bf16_f32 v68, v94, v95
	v_cvt_pk_bf16_f32 v69, v96, v97
	global_store_dwordx4 v[70:71], v[66:69], off offset:256 sc1
	s_cbranch_vccnz .LBB0_162
	s_andn2_b64 vcc, exec, s[22:23]
	s_cbranch_vccnz .LBB0_159
	v_mov_b64_e32 v[68:69], v[64:65]
	v_mov_b64_e32 v[72:73], v[60:61]
	v_mov_b64_e32 v[76:77], v[56:57]
	v_mov_b64_e32 v[80:81], v[52:53]
	s_andn2_b64 vcc, exec, s[20:21]
	v_mov_b64_e32 v[66:67], v[62:63]
	v_mov_b64_e32 v[70:71], v[58:59]
	v_mov_b64_e32 v[74:75], v[54:55]
	v_mov_b64_e32 v[78:79], v[50:51]
	s_cbranch_vccnz .LBB0_158
	v_mul_f32_e32 v67, 0x3d372713, v58
	v_mul_f32_e32 v67, v58, v67
	v_mul_f32_e32 v68, 0x3d372713, v54
	v_fma_f32 v67, v58, v67, v58
	v_mul_f32_e32 v68, v54, v68
	v_mul_f32_e32 v69, 0x3d372713, v50
	v_mul_f32_e32 v67, 0x3fcc422a, v67
	v_fma_f32 v68, v54, v68, v54
	v_mul_f32_e32 v69, v50, v69
	v_mul_f32_e32 v67, 0xbfb8aa3b, v67
	v_mul_f32_e32 v68, 0x3fcc422a, v68
	v_fma_f32 v69, v50, v69, v50
	v_exp_f32_e32 v67, v67
	v_mul_f32_e32 v68, 0xbfb8aa3b, v68
	v_mul_f32_e32 v69, 0x3fcc422a, v69
	v_exp_f32_e32 v68, v68
	v_mul_f32_e32 v69, 0xbfb8aa3b, v69
	v_exp_f32_e32 v69, v69
	v_add_f32_e32 v67, 1.0, v67
	v_rcp_f32_e32 v70, v67
	v_add_f32_e32 v67, 1.0, v68
	v_rcp_f32_e32 v74, v67
	v_add_f32_e32 v67, 1.0, v69
	v_mul_f32_e32 v68, 0x3d372713, v63
	v_mul_f32_e32 v69, 0x3d372713, v59
	v_mul_f32_e32 v68, v63, v68
	v_mul_f32_e32 v69, v59, v69
	v_fma_f32 v68, v63, v68, v63
	v_fma_f32 v69, v59, v69, v59
	v_mul_f32_e32 v68, 0x3fcc422a, v68
	v_mul_f32_e32 v69, 0x3fcc422a, v69
	v_mul_f32_e32 v68, 0xbfb8aa3b, v68
	v_mul_f32_e32 v69, 0xbfb8aa3b, v69
	v_exp_f32_e32 v68, v68
	v_exp_f32_e32 v69, v69
	v_rcp_f32_e32 v78, v67
	v_mul_f32_e32 v71, 0x3d372713, v51
	v_add_f32_e32 v67, 1.0, v68
	v_add_f32_e32 v68, 1.0, v69
	v_mul_f32_e32 v69, 0x3d372713, v55
	v_mul_f32_e32 v69, v55, v69
	v_fma_f32 v69, v55, v69, v55
	v_mul_f32_e32 v71, v51, v71
	v_mul_f32_e32 v69, 0x3fcc422a, v69
	v_fma_f32 v71, v51, v71, v51
	v_mul_f32_e32 v69, 0xbfb8aa3b, v69
	v_mul_f32_e32 v71, 0x3fcc422a, v71
	v_exp_f32_e32 v69, v69
	v_mul_f32_e32 v71, 0xbfb8aa3b, v71
	v_exp_f32_e32 v72, v71
	v_rcp_f32_e32 v71, v68
	v_add_f32_e32 v68, 1.0, v69
	v_rcp_f32_e32 v75, v68
	v_add_f32_e32 v68, 1.0, v72
	v_mul_f32_e32 v69, 0x3d372713, v64
	v_mul_f32_e32 v72, 0x3d372713, v60
	v_mul_f32_e32 v69, v64, v69
	v_mul_f32_e32 v72, v60, v72
	v_fma_f32 v69, v64, v69, v64
	v_fma_f32 v72, v60, v72, v60
	v_mul_f32_e32 v69, 0x3fcc422a, v69
	v_mul_f32_e32 v72, 0x3fcc422a, v72
	v_mul_f32_e32 v69, 0xbfb8aa3b, v69
	v_mul_f32_e32 v72, 0xbfb8aa3b, v72
	v_exp_f32_e32 v69, v69
	v_exp_f32_e32 v72, v72
	v_rcp_f32_e32 v79, v68
	v_mul_f32_e32 v76, 0x3d372713, v65
	v_add_f32_e32 v68, 1.0, v69
	v_add_f32_e32 v69, 1.0, v72
	v_rcp_f32_e32 v72, v69
	v_mul_f32_e32 v69, 0x3d372713, v56
	v_mul_f32_e32 v69, v56, v69
	v_fma_f32 v69, v56, v69, v56
	v_mul_f32_e32 v76, v65, v76
	v_mul_f32_e32 v69, 0x3fcc422a, v69
	v_fma_f32 v76, v65, v76, v65
	v_mul_f32_e32 v69, 0xbfb8aa3b, v69
	v_mul_f32_e32 v76, 0x3fcc422a, v76
	v_exp_f32_e32 v69, v69
	v_mul_f32_e32 v76, 0xbfb8aa3b, v76
	v_exp_f32_e32 v77, v76
	v_mul_f32_e32 v73, 0x3d372713, v52
	v_add_f32_e32 v69, 1.0, v69
	v_mul_f32_e32 v73, v52, v73
	v_rcp_f32_e32 v76, v69
	v_add_f32_e32 v69, 1.0, v77
	v_mul_f32_e32 v77, 0x3d372713, v61
	v_fma_f32 v73, v52, v73, v52
	v_mul_f32_e32 v77, v61, v77
	v_mul_f32_e32 v73, 0x3fcc422a, v73
	v_fma_f32 v77, v61, v77, v61
	v_mul_f32_e32 v73, 0xbfb8aa3b, v73
	v_mul_f32_e32 v77, 0x3fcc422a, v77
	v_exp_f32_e32 v73, v73
	v_mul_f32_e32 v77, 0xbfb8aa3b, v77
	v_exp_f32_e32 v77, v77
	v_mul_f32_e32 v66, 0x3d372713, v62
	v_add_f32_e32 v73, 1.0, v73
	v_rcp_f32_e32 v80, v73
	v_add_f32_e32 v73, 1.0, v77
	v_mul_f32_e32 v77, 0x3d372713, v57
	v_mul_f32_e32 v81, 0x3d372713, v53
	v_mul_f32_e32 v66, v62, v66
	v_mul_f32_e32 v77, v57, v77
	v_mul_f32_e32 v81, v53, v81
	v_fma_f32 v66, v62, v66, v62
	v_fma_f32 v77, v57, v77, v57
	v_fma_f32 v81, v53, v81, v53
	v_mul_f32_e32 v66, 0x3fcc422a, v66
	v_mul_f32_e32 v77, 0x3fcc422a, v77
	v_mul_f32_e32 v81, 0x3fcc422a, v81
	v_mul_f32_e32 v66, 0xbfb8aa3b, v66
	v_mul_f32_e32 v77, 0xbfb8aa3b, v77
	v_mul_f32_e32 v81, 0xbfb8aa3b, v81
	v_exp_f32_e32 v66, v66
	v_exp_f32_e32 v77, v77
	v_exp_f32_e32 v81, v81
	v_rcp_f32_e32 v67, v67
	v_add_f32_e32 v66, 1.0, v66
	v_add_f32_e32 v77, 1.0, v77
	v_add_f32_e32 v81, 1.0, v81
	v_rcp_f32_e32 v66, v66
	v_rcp_f32_e32 v68, v68
	v_rcp_f32_e32 v69, v69
	v_rcp_f32_e32 v73, v73
	v_rcp_f32_e32 v77, v77
	v_rcp_f32_e32 v81, v81
	v_pk_mul_f32 v[68:69], v[64:65], v[68:69]
	v_pk_mul_f32 v[66:67], v[62:63], v[66:67]
	v_pk_mul_f32 v[72:73], v[60:61], v[72:73]
	v_pk_mul_f32 v[70:71], v[58:59], v[70:71]
	v_pk_mul_f32 v[76:77], v[56:57], v[76:77]
	v_pk_mul_f32 v[74:75], v[54:55], v[74:75]
	v_pk_mul_f32 v[80:81], v[52:53], v[80:81]
	v_pk_mul_f32 v[78:79], v[50:51], v[78:79]

.LBB0_164:
	v_mov_b64_e32 v[50:51], s[8:9]
	v_mad_i64_i32 v[50:51], s[24:25], v82, s43, v[50:51]
	v_lshl_add_u64 v[54:55], v[170:171], 1, v[50:51]
	v_cvt_pk_bf16_f32 v50, v66, v67
	v_cvt_pk_bf16_f32 v51, v68, v69
	v_cvt_pk_bf16_f32 v52, v70, v71
	v_cvt_pk_bf16_f32 v53, v72, v73
	global_store_dwordx4 v[54:55], v[50:53], off sc1
	s_and_b64 vcc, exec, s[6:7]
	s_mov_b64 s[24:25], -1
	v_cvt_pk_bf16_f32 v50, v74, v75
	v_cvt_pk_bf16_f32 v51, v76, v77
	v_cvt_pk_bf16_f32 v52, v78, v79
	v_cvt_pk_bf16_f32 v53, v80, v81
	global_store_dwordx4 v[54:55], v[50:53], off offset:256 sc1
	s_cbranch_vccnz .LBB0_172
	s_andn2_b64 vcc, exec, s[22:23]
	s_cbranch_vccnz .LBB0_169
	v_mov_b64_e32 v[52:53], v[48:49]
	v_mov_b64_e32 v[56:57], v[44:45]
	v_mov_b64_e32 v[60:61], v[40:41]
	v_mov_b64_e32 v[64:65], v[36:37]
	s_andn2_b64 vcc, exec, s[20:21]
	v_mov_b64_e32 v[50:51], v[46:47]
	v_mov_b64_e32 v[54:55], v[42:43]
	v_mov_b64_e32 v[58:59], v[38:39]
	v_mov_b64_e32 v[62:63], v[34:35]
	s_cbranch_vccnz .LBB0_168
	v_mul_f32_e32 v51, 0x3d372713, v42
	v_mul_f32_e32 v51, v42, v51
	v_mul_f32_e32 v52, 0x3d372713, v38
	v_fma_f32 v51, v42, v51, v42
	v_mul_f32_e32 v52, v38, v52
	v_mul_f32_e32 v53, 0x3d372713, v34
	v_mul_f32_e32 v51, 0x3fcc422a, v51
	v_fma_f32 v52, v38, v52, v38
	v_mul_f32_e32 v53, v34, v53
	v_mul_f32_e32 v51, 0xbfb8aa3b, v51
	v_mul_f32_e32 v52, 0x3fcc422a, v52
	v_fma_f32 v53, v34, v53, v34
	v_exp_f32_e32 v51, v51
	v_mul_f32_e32 v52, 0xbfb8aa3b, v52
	v_mul_f32_e32 v53, 0x3fcc422a, v53
	v_exp_f32_e32 v52, v52
	v_mul_f32_e32 v53, 0xbfb8aa3b, v53
	v_exp_f32_e32 v53, v53
	v_add_f32_e32 v51, 1.0, v51
	v_rcp_f32_e32 v54, v51
	v_add_f32_e32 v51, 1.0, v52
	v_rcp_f32_e32 v58, v51
	v_add_f32_e32 v51, 1.0, v53
	v_mul_f32_e32 v52, 0x3d372713, v47
	v_mul_f32_e32 v53, 0x3d372713, v43
	v_mul_f32_e32 v52, v47, v52
	v_mul_f32_e32 v53, v43, v53
	v_fma_f32 v52, v47, v52, v47
	v_fma_f32 v53, v43, v53, v43
	v_mul_f32_e32 v52, 0x3fcc422a, v52
	v_mul_f32_e32 v53, 0x3fcc422a, v53
	v_mul_f32_e32 v52, 0xbfb8aa3b, v52
	v_mul_f32_e32 v53, 0xbfb8aa3b, v53
	v_exp_f32_e32 v52, v52
	v_exp_f32_e32 v53, v53
	v_rcp_f32_e32 v62, v51
	v_mul_f32_e32 v55, 0x3d372713, v35
	v_add_f32_e32 v51, 1.0, v52
	v_add_f32_e32 v52, 1.0, v53
	v_mul_f32_e32 v53, 0x3d372713, v39
	v_mul_f32_e32 v53, v39, v53
	v_fma_f32 v53, v39, v53, v39
	v_mul_f32_e32 v55, v35, v55
	v_mul_f32_e32 v53, 0x3fcc422a, v53
	v_fma_f32 v55, v35, v55, v35
	v_mul_f32_e32 v53, 0xbfb8aa3b, v53
	v_mul_f32_e32 v55, 0x3fcc422a, v55
	v_exp_f32_e32 v53, v53
	v_mul_f32_e32 v55, 0xbfb8aa3b, v55
	v_exp_f32_e32 v56, v55
	v_rcp_f32_e32 v55, v52
	v_add_f32_e32 v52, 1.0, v53
	v_rcp_f32_e32 v59, v52
	v_add_f32_e32 v52, 1.0, v56
	v_mul_f32_e32 v53, 0x3d372713, v48
	v_mul_f32_e32 v56, 0x3d372713, v44
	v_mul_f32_e32 v53, v48, v53
	v_mul_f32_e32 v56, v44, v56
	v_fma_f32 v53, v48, v53, v48
	v_fma_f32 v56, v44, v56, v44
	v_mul_f32_e32 v53, 0x3fcc422a, v53
	v_mul_f32_e32 v56, 0x3fcc422a, v56
	v_mul_f32_e32 v53, 0xbfb8aa3b, v53
	v_mul_f32_e32 v56, 0xbfb8aa3b, v56
	v_exp_f32_e32 v53, v53
	v_exp_f32_e32 v56, v56
	v_rcp_f32_e32 v63, v52
	v_mul_f32_e32 v60, 0x3d372713, v49
	v_add_f32_e32 v52, 1.0, v53
	v_add_f32_e32 v53, 1.0, v56
	v_rcp_f32_e32 v56, v53
	v_mul_f32_e32 v53, 0x3d372713, v40
	v_mul_f32_e32 v53, v40, v53
	v_fma_f32 v53, v40, v53, v40
	v_mul_f32_e32 v60, v49, v60
	v_mul_f32_e32 v53, 0x3fcc422a, v53
	v_fma_f32 v60, v49, v60, v49
	v_mul_f32_e32 v53, 0xbfb8aa3b, v53
	v_mul_f32_e32 v60, 0x3fcc422a, v60
	v_exp_f32_e32 v53, v53
	v_mul_f32_e32 v60, 0xbfb8aa3b, v60
	v_exp_f32_e32 v61, v60
	v_mul_f32_e32 v57, 0x3d372713, v36
	v_add_f32_e32 v53, 1.0, v53
	v_mul_f32_e32 v57, v36, v57
	v_rcp_f32_e32 v60, v53
	v_add_f32_e32 v53, 1.0, v61
	v_mul_f32_e32 v61, 0x3d372713, v45
	v_fma_f32 v57, v36, v57, v36
	v_mul_f32_e32 v61, v45, v61
	v_mul_f32_e32 v57, 0x3fcc422a, v57
	v_fma_f32 v61, v45, v61, v45
	v_mul_f32_e32 v57, 0xbfb8aa3b, v57
	v_mul_f32_e32 v61, 0x3fcc422a, v61
	v_exp_f32_e32 v57, v57
	v_mul_f32_e32 v61, 0xbfb8aa3b, v61
	v_exp_f32_e32 v61, v61
	v_mul_f32_e32 v50, 0x3d372713, v46
	v_add_f32_e32 v57, 1.0, v57
	v_rcp_f32_e32 v64, v57
	v_add_f32_e32 v57, 1.0, v61
	v_mul_f32_e32 v61, 0x3d372713, v41
	v_mul_f32_e32 v65, 0x3d372713, v37
	v_mul_f32_e32 v50, v46, v50
	v_mul_f32_e32 v61, v41, v61
	v_mul_f32_e32 v65, v37, v65
	v_fma_f32 v50, v46, v50, v46
	v_fma_f32 v61, v41, v61, v41
	v_fma_f32 v65, v37, v65, v37
	v_mul_f32_e32 v50, 0x3fcc422a, v50
	v_mul_f32_e32 v61, 0x3fcc422a, v61
	v_mul_f32_e32 v65, 0x3fcc422a, v65
	v_mul_f32_e32 v50, 0xbfb8aa3b, v50
	v_mul_f32_e32 v61, 0xbfb8aa3b, v61
	v_mul_f32_e32 v65, 0xbfb8aa3b, v65
	v_exp_f32_e32 v50, v50
	v_exp_f32_e32 v61, v61
	v_exp_f32_e32 v65, v65
	v_rcp_f32_e32 v51, v51
	v_add_f32_e32 v50, 1.0, v50
	v_add_f32_e32 v61, 1.0, v61
	v_add_f32_e32 v65, 1.0, v65
	v_rcp_f32_e32 v50, v50
	v_rcp_f32_e32 v52, v52
	v_rcp_f32_e32 v53, v53
	v_rcp_f32_e32 v57, v57
	v_rcp_f32_e32 v61, v61
	v_rcp_f32_e32 v65, v65
	v_pk_mul_f32 v[52:53], v[48:49], v[52:53]
	v_pk_mul_f32 v[50:51], v[46:47], v[50:51]
	v_pk_mul_f32 v[56:57], v[44:45], v[56:57]
	v_pk_mul_f32 v[54:55], v[42:43], v[54:55]
	v_pk_mul_f32 v[60:61], v[40:41], v[60:61]
	v_pk_mul_f32 v[58:59], v[38:39], v[58:59]
	v_pk_mul_f32 v[64:65], v[36:37], v[64:65]
	v_pk_mul_f32 v[62:63], v[34:35], v[62:63]

.LBB0_174:
	v_mov_b64_e32 v[34:35], s[8:9]
	v_mad_i64_i32 v[34:35], s[24:25], v66, s43, v[34:35]
	v_lshl_add_u64 v[38:39], v[170:171], 1, v[34:35]
	v_cvt_pk_bf16_f32 v34, v50, v51
	v_cvt_pk_bf16_f32 v35, v52, v53
	v_cvt_pk_bf16_f32 v36, v54, v55
	v_cvt_pk_bf16_f32 v37, v56, v57
	global_store_dwordx4 v[38:39], v[34:37], off sc1
	s_and_b64 vcc, exec, s[6:7]
	s_mov_b64 s[24:25], -1
	v_cvt_pk_bf16_f32 v34, v58, v59
	v_cvt_pk_bf16_f32 v35, v60, v61
	v_cvt_pk_bf16_f32 v36, v62, v63
	v_cvt_pk_bf16_f32 v37, v64, v65
	global_store_dwordx4 v[38:39], v[34:37], off offset:256 sc1
	s_cbranch_vccnz .LBB0_182
	s_andn2_b64 vcc, exec, s[22:23]
	s_cbranch_vccnz .LBB0_179
	v_mov_b64_e32 v[36:37], v[32:33]
	v_mov_b64_e32 v[40:41], v[28:29]
	v_mov_b64_e32 v[44:45], v[24:25]
	v_mov_b64_e32 v[48:49], v[20:21]
	s_andn2_b64 vcc, exec, s[20:21]
	v_mov_b64_e32 v[34:35], v[30:31]
	v_mov_b64_e32 v[38:39], v[26:27]
	v_mov_b64_e32 v[42:43], v[22:23]
	v_mov_b64_e32 v[46:47], v[18:19]
	s_cbranch_vccnz .LBB0_178
	v_mul_f32_e32 v35, 0x3d372713, v26
	v_mul_f32_e32 v35, v26, v35
	v_mul_f32_e32 v36, 0x3d372713, v22
	v_fma_f32 v35, v26, v35, v26
	v_mul_f32_e32 v36, v22, v36
	v_mul_f32_e32 v37, 0x3d372713, v18
	v_mul_f32_e32 v35, 0x3fcc422a, v35
	v_fma_f32 v36, v22, v36, v22
	v_mul_f32_e32 v37, v18, v37
	v_mul_f32_e32 v35, 0xbfb8aa3b, v35
	v_mul_f32_e32 v36, 0x3fcc422a, v36
	v_fma_f32 v37, v18, v37, v18
	v_exp_f32_e32 v35, v35
	v_mul_f32_e32 v36, 0xbfb8aa3b, v36
	v_mul_f32_e32 v37, 0x3fcc422a, v37
	v_exp_f32_e32 v36, v36
	v_mul_f32_e32 v37, 0xbfb8aa3b, v37
	v_exp_f32_e32 v37, v37
	v_add_f32_e32 v35, 1.0, v35
	v_rcp_f32_e32 v38, v35
	v_add_f32_e32 v35, 1.0, v36
	v_rcp_f32_e32 v42, v35
	v_add_f32_e32 v35, 1.0, v37
	v_mul_f32_e32 v36, 0x3d372713, v31
	v_mul_f32_e32 v37, 0x3d372713, v27
	v_mul_f32_e32 v36, v31, v36
	v_mul_f32_e32 v37, v27, v37
	v_fma_f32 v36, v31, v36, v31
	v_fma_f32 v37, v27, v37, v27
	v_mul_f32_e32 v36, 0x3fcc422a, v36
	v_mul_f32_e32 v37, 0x3fcc422a, v37
	v_mul_f32_e32 v36, 0xbfb8aa3b, v36
	v_mul_f32_e32 v37, 0xbfb8aa3b, v37
	v_exp_f32_e32 v36, v36
	v_exp_f32_e32 v37, v37
	v_rcp_f32_e32 v46, v35
	v_mul_f32_e32 v39, 0x3d372713, v19
	v_add_f32_e32 v35, 1.0, v36
	v_add_f32_e32 v36, 1.0, v37
	v_mul_f32_e32 v37, 0x3d372713, v23
	v_mul_f32_e32 v37, v23, v37
	v_fma_f32 v37, v23, v37, v23
	v_mul_f32_e32 v39, v19, v39
	v_mul_f32_e32 v37, 0x3fcc422a, v37
	v_fma_f32 v39, v19, v39, v19
	v_mul_f32_e32 v37, 0xbfb8aa3b, v37
	v_mul_f32_e32 v39, 0x3fcc422a, v39
	v_exp_f32_e32 v37, v37
	v_mul_f32_e32 v39, 0xbfb8aa3b, v39
	v_exp_f32_e32 v40, v39
	v_rcp_f32_e32 v39, v36
	v_add_f32_e32 v36, 1.0, v37
	v_rcp_f32_e32 v43, v36
	v_add_f32_e32 v36, 1.0, v40
	v_mul_f32_e32 v37, 0x3d372713, v32
	v_mul_f32_e32 v40, 0x3d372713, v28
	v_mul_f32_e32 v37, v32, v37
	v_mul_f32_e32 v40, v28, v40
	v_fma_f32 v37, v32, v37, v32
	v_fma_f32 v40, v28, v40, v28
	v_mul_f32_e32 v37, 0x3fcc422a, v37
	v_mul_f32_e32 v40, 0x3fcc422a, v40
	v_mul_f32_e32 v37, 0xbfb8aa3b, v37
	v_mul_f32_e32 v40, 0xbfb8aa3b, v40
	v_exp_f32_e32 v37, v37
	v_exp_f32_e32 v40, v40
	v_rcp_f32_e32 v47, v36
	v_mul_f32_e32 v44, 0x3d372713, v33
	v_add_f32_e32 v36, 1.0, v37
	v_add_f32_e32 v37, 1.0, v40
	v_rcp_f32_e32 v40, v37
	v_mul_f32_e32 v37, 0x3d372713, v24
	v_mul_f32_e32 v37, v24, v37
	v_fma_f32 v37, v24, v37, v24
	v_mul_f32_e32 v44, v33, v44
	v_mul_f32_e32 v37, 0x3fcc422a, v37
	v_fma_f32 v44, v33, v44, v33
	v_mul_f32_e32 v37, 0xbfb8aa3b, v37
	v_mul_f32_e32 v44, 0x3fcc422a, v44
	v_exp_f32_e32 v37, v37
	v_mul_f32_e32 v44, 0xbfb8aa3b, v44
	v_exp_f32_e32 v45, v44
	v_mul_f32_e32 v41, 0x3d372713, v20
	v_add_f32_e32 v37, 1.0, v37
	v_mul_f32_e32 v41, v20, v41
	v_rcp_f32_e32 v44, v37
	v_add_f32_e32 v37, 1.0, v45
	v_mul_f32_e32 v45, 0x3d372713, v29
	v_fma_f32 v41, v20, v41, v20
	v_mul_f32_e32 v45, v29, v45
	v_mul_f32_e32 v41, 0x3fcc422a, v41
	v_fma_f32 v45, v29, v45, v29
	v_mul_f32_e32 v41, 0xbfb8aa3b, v41
	v_mul_f32_e32 v45, 0x3fcc422a, v45
	v_exp_f32_e32 v41, v41
	v_mul_f32_e32 v45, 0xbfb8aa3b, v45
	v_exp_f32_e32 v45, v45
	v_mul_f32_e32 v34, 0x3d372713, v30
	v_add_f32_e32 v41, 1.0, v41
	v_rcp_f32_e32 v48, v41
	v_add_f32_e32 v41, 1.0, v45
	v_mul_f32_e32 v45, 0x3d372713, v25
	v_mul_f32_e32 v49, 0x3d372713, v21
	v_mul_f32_e32 v34, v30, v34
	v_mul_f32_e32 v45, v25, v45
	v_mul_f32_e32 v49, v21, v49
	v_fma_f32 v34, v30, v34, v30
	v_fma_f32 v45, v25, v45, v25
	v_fma_f32 v49, v21, v49, v21
	v_mul_f32_e32 v34, 0x3fcc422a, v34
	v_mul_f32_e32 v45, 0x3fcc422a, v45
	v_mul_f32_e32 v49, 0x3fcc422a, v49
	v_mul_f32_e32 v34, 0xbfb8aa3b, v34
	v_mul_f32_e32 v45, 0xbfb8aa3b, v45
	v_mul_f32_e32 v49, 0xbfb8aa3b, v49
	v_exp_f32_e32 v34, v34
	v_exp_f32_e32 v45, v45
	v_exp_f32_e32 v49, v49
	v_rcp_f32_e32 v35, v35
	v_add_f32_e32 v34, 1.0, v34
	v_add_f32_e32 v45, 1.0, v45
	v_add_f32_e32 v49, 1.0, v49
	v_rcp_f32_e32 v34, v34
	v_rcp_f32_e32 v36, v36
	v_rcp_f32_e32 v37, v37
	v_rcp_f32_e32 v41, v41
	v_rcp_f32_e32 v45, v45
	v_rcp_f32_e32 v49, v49
	v_pk_mul_f32 v[36:37], v[32:33], v[36:37]
	v_pk_mul_f32 v[34:35], v[30:31], v[34:35]
	v_pk_mul_f32 v[40:41], v[28:29], v[40:41]
	v_pk_mul_f32 v[38:39], v[26:27], v[38:39]
	v_pk_mul_f32 v[44:45], v[24:25], v[44:45]
	v_pk_mul_f32 v[42:43], v[22:23], v[42:43]
	v_pk_mul_f32 v[48:49], v[20:21], v[48:49]
	v_pk_mul_f32 v[46:47], v[18:19], v[46:47]

.LBB0_184:
	v_mov_b64_e32 v[18:19], s[8:9]
	v_mad_i64_i32 v[18:19], s[24:25], v50, s43, v[18:19]
	v_lshl_add_u64 v[22:23], v[170:171], 1, v[18:19]
	v_cvt_pk_bf16_f32 v18, v34, v35
	v_cvt_pk_bf16_f32 v19, v36, v37
	v_cvt_pk_bf16_f32 v20, v38, v39
	v_cvt_pk_bf16_f32 v21, v40, v41
	global_store_dwordx4 v[22:23], v[18:21], off sc1
	s_and_b64 vcc, exec, s[6:7]
	s_mov_b64 s[6:7], -1
	v_cvt_pk_bf16_f32 v18, v42, v43
	v_cvt_pk_bf16_f32 v19, v44, v45
	v_cvt_pk_bf16_f32 v20, v46, v47
	v_cvt_pk_bf16_f32 v21, v48, v49
	global_store_dwordx4 v[22:23], v[18:21], off offset:256 sc1
	s_cbranch_vccnz .LBB0_192
	s_andn2_b64 vcc, exec, s[22:23]
	s_cbranch_vccnz .LBB0_189
	v_mov_b64_e32 v[20:21], v[16:17]
	v_mov_b64_e32 v[24:25], v[12:13]
	v_mov_b64_e32 v[28:29], v[8:9]
	v_mov_b64_e32 v[32:33], v[4:5]
	s_andn2_b64 vcc, exec, s[20:21]
	v_mov_b64_e32 v[18:19], v[14:15]
	v_mov_b64_e32 v[22:23], v[10:11]
	v_mov_b64_e32 v[26:27], v[6:7]
	v_mov_b64_e32 v[30:31], v[2:3]
	s_cbranch_vccnz .LBB0_188
	v_mul_f32_e32 v19, 0x3d372713, v10
	v_mul_f32_e32 v19, v10, v19
	v_mul_f32_e32 v20, 0x3d372713, v6
	v_fma_f32 v19, v10, v19, v10
	v_mul_f32_e32 v20, v6, v20
	v_mul_f32_e32 v21, 0x3d372713, v2
	v_mul_f32_e32 v19, 0x3fcc422a, v19
	v_fma_f32 v20, v6, v20, v6
	v_mul_f32_e32 v21, v2, v21
	v_mul_f32_e32 v19, 0xbfb8aa3b, v19
	v_mul_f32_e32 v20, 0x3fcc422a, v20
	v_fma_f32 v21, v2, v21, v2
	v_exp_f32_e32 v19, v19
	v_mul_f32_e32 v20, 0xbfb8aa3b, v20
	v_mul_f32_e32 v21, 0x3fcc422a, v21
	v_exp_f32_e32 v20, v20
	v_mul_f32_e32 v21, 0xbfb8aa3b, v21
	v_exp_f32_e32 v21, v21
	v_add_f32_e32 v19, 1.0, v19
	v_rcp_f32_e32 v22, v19
	v_add_f32_e32 v19, 1.0, v20
	v_rcp_f32_e32 v26, v19
	v_add_f32_e32 v19, 1.0, v21
	v_mul_f32_e32 v20, 0x3d372713, v15
	v_mul_f32_e32 v21, 0x3d372713, v11
	v_mul_f32_e32 v20, v15, v20
	v_mul_f32_e32 v21, v11, v21
	v_fma_f32 v20, v15, v20, v15
	v_fma_f32 v21, v11, v21, v11
	v_mul_f32_e32 v20, 0x3fcc422a, v20
	v_mul_f32_e32 v21, 0x3fcc422a, v21
	v_mul_f32_e32 v20, 0xbfb8aa3b, v20
	v_mul_f32_e32 v21, 0xbfb8aa3b, v21
	v_exp_f32_e32 v20, v20
	v_exp_f32_e32 v21, v21
	v_rcp_f32_e32 v30, v19
	v_mul_f32_e32 v23, 0x3d372713, v3
	v_add_f32_e32 v19, 1.0, v20
	v_add_f32_e32 v20, 1.0, v21
	v_mul_f32_e32 v21, 0x3d372713, v7
	v_mul_f32_e32 v21, v7, v21
	v_fma_f32 v21, v7, v21, v7
	v_mul_f32_e32 v23, v3, v23
	v_mul_f32_e32 v21, 0x3fcc422a, v21
	v_fma_f32 v23, v3, v23, v3
	v_mul_f32_e32 v21, 0xbfb8aa3b, v21
	v_mul_f32_e32 v23, 0x3fcc422a, v23
	v_exp_f32_e32 v21, v21
	v_mul_f32_e32 v23, 0xbfb8aa3b, v23
	v_exp_f32_e32 v24, v23
	v_rcp_f32_e32 v23, v20
	v_add_f32_e32 v20, 1.0, v21
	v_rcp_f32_e32 v27, v20
	v_add_f32_e32 v20, 1.0, v24
	v_mul_f32_e32 v21, 0x3d372713, v16
	v_mul_f32_e32 v24, 0x3d372713, v12
	v_mul_f32_e32 v21, v16, v21
	v_mul_f32_e32 v24, v12, v24
	v_fma_f32 v21, v16, v21, v16
	v_fma_f32 v24, v12, v24, v12
	v_mul_f32_e32 v21, 0x3fcc422a, v21
	v_mul_f32_e32 v24, 0x3fcc422a, v24
	v_mul_f32_e32 v21, 0xbfb8aa3b, v21
	v_mul_f32_e32 v24, 0xbfb8aa3b, v24
	v_exp_f32_e32 v21, v21
	v_exp_f32_e32 v24, v24
	v_rcp_f32_e32 v31, v20
	v_mul_f32_e32 v28, 0x3d372713, v17
	v_add_f32_e32 v20, 1.0, v21
	v_add_f32_e32 v21, 1.0, v24
	v_rcp_f32_e32 v24, v21
	v_mul_f32_e32 v21, 0x3d372713, v8
	v_mul_f32_e32 v21, v8, v21
	v_fma_f32 v21, v8, v21, v8
	v_mul_f32_e32 v28, v17, v28
	v_mul_f32_e32 v21, 0x3fcc422a, v21
	v_fma_f32 v28, v17, v28, v17
	v_mul_f32_e32 v21, 0xbfb8aa3b, v21
	v_mul_f32_e32 v28, 0x3fcc422a, v28
	v_exp_f32_e32 v21, v21
	v_mul_f32_e32 v28, 0xbfb8aa3b, v28
	v_exp_f32_e32 v29, v28
	v_mul_f32_e32 v25, 0x3d372713, v4
	v_add_f32_e32 v21, 1.0, v21
	v_mul_f32_e32 v25, v4, v25
	v_rcp_f32_e32 v28, v21
	v_add_f32_e32 v21, 1.0, v29
	v_mul_f32_e32 v29, 0x3d372713, v13
	v_fma_f32 v25, v4, v25, v4
	v_mul_f32_e32 v29, v13, v29
	v_mul_f32_e32 v25, 0x3fcc422a, v25
	v_fma_f32 v29, v13, v29, v13
	v_mul_f32_e32 v25, 0xbfb8aa3b, v25
	v_mul_f32_e32 v29, 0x3fcc422a, v29
	v_exp_f32_e32 v25, v25
	v_mul_f32_e32 v29, 0xbfb8aa3b, v29
	v_exp_f32_e32 v29, v29
	v_mul_f32_e32 v18, 0x3d372713, v14
	v_add_f32_e32 v25, 1.0, v25
	v_rcp_f32_e32 v32, v25
	v_add_f32_e32 v25, 1.0, v29
	v_mul_f32_e32 v29, 0x3d372713, v9
	v_mul_f32_e32 v33, 0x3d372713, v5
	v_mul_f32_e32 v18, v14, v18
	v_mul_f32_e32 v29, v9, v29
	v_mul_f32_e32 v33, v5, v33
	v_fma_f32 v18, v14, v18, v14
	v_fma_f32 v29, v9, v29, v9
	v_fma_f32 v33, v5, v33, v5
	v_mul_f32_e32 v18, 0x3fcc422a, v18
	v_mul_f32_e32 v29, 0x3fcc422a, v29
	v_mul_f32_e32 v33, 0x3fcc422a, v33
	v_mul_f32_e32 v18, 0xbfb8aa3b, v18
	v_mul_f32_e32 v29, 0xbfb8aa3b, v29
	v_mul_f32_e32 v33, 0xbfb8aa3b, v33
	v_exp_f32_e32 v18, v18
	v_exp_f32_e32 v29, v29
	v_exp_f32_e32 v33, v33
	v_rcp_f32_e32 v19, v19
	v_add_f32_e32 v18, 1.0, v18
	v_add_f32_e32 v29, 1.0, v29
	v_add_f32_e32 v33, 1.0, v33
	v_rcp_f32_e32 v18, v18
	v_rcp_f32_e32 v20, v20
	v_rcp_f32_e32 v21, v21
	v_rcp_f32_e32 v25, v25
	v_rcp_f32_e32 v29, v29
	v_rcp_f32_e32 v33, v33
	v_pk_mul_f32 v[20:21], v[16:17], v[20:21]
	v_pk_mul_f32 v[18:19], v[14:15], v[18:19]
	v_pk_mul_f32 v[24:25], v[12:13], v[24:25]
	v_pk_mul_f32 v[22:23], v[10:11], v[22:23]
	v_pk_mul_f32 v[28:29], v[8:9], v[28:29]
	v_pk_mul_f32 v[26:27], v[6:7], v[26:27]
	v_pk_mul_f32 v[32:33], v[4:5], v[32:33]
	v_pk_mul_f32 v[30:31], v[2:3], v[30:31]

.LBB0_194:
	v_mov_b64_e32 v[2:3], s[8:9]
	v_mad_i64_i32 v[2:3], s[6:7], v34, s43, v[2:3]
	v_lshl_add_u64 v[6:7], v[170:171], 1, v[2:3]
	v_cvt_pk_bf16_f32 v2, v18, v19
	v_cvt_pk_bf16_f32 v3, v20, v21
	v_cvt_pk_bf16_f32 v4, v22, v23
	v_cvt_pk_bf16_f32 v5, v24, v25
	s_andn2_b64 vcc, exec, s[4:5]
	s_mov_b64 s[4:5], -1
	global_store_dwordx4 v[6:7], v[2:5], off sc1
	s_nop 1
	v_cvt_pk_bf16_f32 v2, v26, v27
	v_cvt_pk_bf16_f32 v3, v28, v29
	v_cvt_pk_bf16_f32 v4, v30, v31
	v_cvt_pk_bf16_f32 v5, v32, v33
	global_store_dwordx4 v[6:7], v[2:5], off offset:256 sc1
	s_cbranch_vccnz .LBB0_107
	s_andn2_b64 vcc, exec, s[0:1]
	s_cbranch_vccnz .LBB0_106
	s_barrier
	s_branch .LBB0_106

.LBB0_457:
	s_lshl_b32 s36, s36, 8
	v_add_u32_e32 v152, s36, v155
	v_lshl_or_b32 v150, s37, 8, v157
	v_ashrrev_i32_e32 v153, 31, v152
	v_ashrrev_i32_e32 v151, 31, v150
	v_lshlrev_b64 v[162:163], 12, v[152:153]
	v_lshl_add_u64 v[170:171], v[162:163], 0, v[150:151]
	v_lshl_add_u64 v[172:173], v[170:171], 2, s[0:1]
	global_load_dwordx4 v[162:165], v[172:173], off
	global_load_dwordx4 v[166:169], v[172:173], off offset:16
	v_lshl_add_u64 v[170:171], v[170:171], 1, s[10:11]
	v_xor_b32_e32 v149, 32, v161
	s_waitcnt vmcnt(0)
	v_pk_add_f32 v[128:129], v[128:129], v[164:165]
	v_pk_add_f32 v[126:127], v[126:127], v[162:163]
	v_pk_add_f32 v[124:125], v[124:125], v[168:169]
	v_pk_add_f32 v[122:123], v[122:123], v[166:167]
	v_cvt_pk_bf16_f32 v162, v126, v127
	v_cvt_pk_bf16_f32 v163, v128, v129
	v_mul_f32_e32 v127, v127, v127
	v_cvt_pk_bf16_f32 v164, v122, v123
	v_cvt_pk_bf16_f32 v165, v124, v125
	global_store_dwordx4 v[170:171], v[162:165], off sc1
	global_load_dwordx4 v[162:165], v[172:173], off offset:512
	s_nop 0
	global_load_dwordx4 v[166:169], v[172:173], off offset:528
	v_or_b32_e32 v172, 16, v152
	v_ashrrev_i32_e32 v173, 31, v172
	v_lshlrev_b64 v[172:173], 12, v[172:173]
	v_lshl_add_u64 v[172:173], v[172:173], 0, v[150:151]
	v_lshl_add_u64 v[174:175], v[172:173], 2, s[0:1]
	v_mul_f32_e32 v129, v129, v129
	v_mul_f32_e32 v123, v123, v123
	v_mul_f32_e32 v125, v125, v125
	v_fmac_f32_e32 v127, v126, v126
	v_fmac_f32_e32 v129, v128, v128
	v_fmac_f32_e32 v123, v122, v122
	v_fmac_f32_e32 v125, v124, v124
	v_add_f32_e32 v126, v127, v129
	v_add_f32_e32 v127, v123, v125
	s_waitcnt vmcnt(1)
	v_pk_add_f32 v[120:121], v[120:121], v[164:165]
	v_pk_add_f32 v[118:119], v[118:119], v[162:163]
	s_waitcnt vmcnt(0)
	v_pk_add_f32 v[116:117], v[116:117], v[168:169]
	v_pk_add_f32 v[114:115], v[114:115], v[166:167]
	v_cvt_pk_bf16_f32 v162, v118, v119
	v_cvt_pk_bf16_f32 v163, v120, v121
	s_nop 0
	v_cvt_pk_bf16_f32 v164, v114, v115
	v_cvt_pk_bf16_f32 v165, v116, v117
	global_store_dwordx4 v[170:171], v[162:165], off offset:256 sc1
	global_load_dwordx4 v[162:165], v[174:175], off
	s_nop 0
	global_load_dwordx4 v[166:169], v[174:175], off offset:16
	v_lshl_add_u64 v[170:171], v[172:173], 1, s[10:11]
	v_or_b32_e32 v172, 32, v152
	v_ashrrev_i32_e32 v173, 31, v172
	v_lshlrev_b64 v[172:173], 12, v[172:173]
	v_lshl_add_u64 v[172:173], v[172:173], 0, v[150:151]
	s_waitcnt vmcnt(1)
	v_pk_add_f32 v[112:113], v[112:113], v[164:165]
	v_pk_add_f32 v[110:111], v[110:111], v[162:163]
	s_waitcnt vmcnt(0)
	v_pk_add_f32 v[108:109], v[108:109], v[168:169]
	v_pk_add_f32 v[106:107], v[106:107], v[166:167]
	v_cvt_pk_bf16_f32 v162, v110, v111
	v_cvt_pk_bf16_f32 v163, v112, v113
	s_nop 0
	v_cvt_pk_bf16_f32 v164, v106, v107
	v_cvt_pk_bf16_f32 v165, v108, v109
	global_store_dwordx4 v[170:171], v[162:165], off sc1
	global_load_dwordx4 v[162:165], v[174:175], off offset:512
	s_nop 0
	global_load_dwordx4 v[166:169], v[174:175], off offset:528
	v_lshl_add_u64 v[174:175], v[172:173], 2, s[0:1]
	v_mul_f32_e32 v107, v107, v107
	v_mul_f32_e32 v109, v109, v109
	v_fmac_f32_e32 v107, v106, v106
	v_fmac_f32_e32 v109, v108, v108
	s_waitcnt vmcnt(1)
	v_pk_add_f32 v[164:165], v[104:105], v[164:165]
	v_pk_add_f32 v[162:163], v[102:103], v[162:163]
	s_waitcnt vmcnt(0)
	v_pk_add_f32 v[168:169], v[100:101], v[168:169]
	v_pk_add_f32 v[166:167], v[98:99], v[166:167]
	v_cvt_pk_bf16_f32 v98, v162, v163
	v_cvt_pk_bf16_f32 v99, v164, v165
	v_mul_f32_e32 v106, v165, v165
	v_cvt_pk_bf16_f32 v100, v166, v167
	v_cvt_pk_bf16_f32 v101, v168, v169
	global_store_dwordx4 v[170:171], v[98:101], off offset:256 sc1
	global_load_dwordx4 v[98:101], v[174:175], off
	s_nop 0
	global_load_dwordx4 v[102:105], v[174:175], off offset:16
	v_lshl_add_u64 v[170:171], v[172:173], 1, s[10:11]
	v_or_b32_e32 v172, 48, v152
	v_ashrrev_i32_e32 v173, 31, v172
	v_lshlrev_b64 v[172:173], 12, v[172:173]
	v_lshl_add_u64 v[172:173], v[172:173], 0, v[150:151]
	v_mul_f32_e32 v108, v169, v169
	v_fmac_f32_e32 v106, v164, v164
	v_fmac_f32_e32 v108, v168, v168
	s_waitcnt vmcnt(1)
	v_pk_add_f32 v[100:101], v[96:97], v[100:101]
	v_pk_add_f32 v[98:99], v[94:95], v[98:99]
	s_waitcnt vmcnt(0)
	v_pk_add_f32 v[104:105], v[92:93], v[104:105]
	v_pk_add_f32 v[102:103], v[90:91], v[102:103]
	v_cvt_pk_bf16_f32 v90, v98, v99
	v_cvt_pk_bf16_f32 v91, v100, v101
	s_nop 0
	v_cvt_pk_bf16_f32 v92, v102, v103
	v_cvt_pk_bf16_f32 v93, v104, v105
	global_store_dwordx4 v[170:171], v[90:93], off sc1
	global_load_dwordx4 v[90:93], v[174:175], off offset:512
	s_nop 0
	global_load_dwordx4 v[94:97], v[174:175], off offset:528
	v_lshl_add_u64 v[174:175], v[172:173], 2, s[0:1]
	s_waitcnt vmcnt(1)
	v_pk_add_f32 v[92:93], v[88:89], v[92:93]
	v_pk_add_f32 v[176:177], v[86:87], v[90:91]
	s_waitcnt vmcnt(0)
	v_pk_add_f32 v[96:97], v[84:85], v[96:97]
	v_pk_add_f32 v[94:95], v[82:83], v[94:95]
	v_cvt_pk_bf16_f32 v82, v176, v177
	v_cvt_pk_bf16_f32 v83, v92, v93
	v_mul_f32_e32 v93, v93, v93
	v_cvt_pk_bf16_f32 v84, v94, v95
	v_cvt_pk_bf16_f32 v85, v96, v97
	global_store_dwordx4 v[170:171], v[82:85], off offset:256 sc1
	global_load_dwordx4 v[84:87], v[174:175], off
	s_nop 0
	global_load_dwordx4 v[88:91], v[174:175], off offset:16
	v_lshl_add_u64 v[170:171], v[172:173], 1, s[10:11]
	v_and_b32_e32 v83, 64, v161
	v_xor_b32_e32 v82, 16, v161
	v_add_u32_e32 v83, 64, v83
	v_cmp_lt_i32_e32 vcc, v82, v83
	v_mul_f32_e32 v95, v95, v95
	v_mul_f32_e32 v97, v97, v97
	v_cndmask_b32_e32 v82, v161, v82, vcc
	v_cmp_lt_i32_e32 vcc, v149, v83
	v_mul_f32_e32 v83, v99, v99
	v_mul_f32_e32 v99, v101, v101
	v_mul_f32_e32 v101, v103, v103
	v_mul_f32_e32 v103, v105, v105
	v_fmac_f32_e32 v83, v98, v98
	v_fmac_f32_e32 v99, v100, v100
	v_fmac_f32_e32 v101, v102, v102
	v_fmac_f32_e32 v103, v104, v104
	v_add_f32_e32 v83, v83, v99
	v_add_f32_e32 v98, v101, v103
	v_add_f32_e32 v83, v83, v98
	v_mul_f32_e32 v98, v177, v177
	v_fmac_f32_e32 v98, v176, v176
	v_fmac_f32_e32 v93, v92, v92
	v_fmac_f32_e32 v95, v94, v94
	v_fmac_f32_e32 v97, v96, v96
	v_add_f32_e32 v92, v98, v93
	v_add_f32_e32 v93, v95, v97
	v_add_f32_e32 v92, v92, v93
	v_lshlrev_b32_e32 v82, 2, v82
	v_add_f32_e32 v83, v83, v92
	ds_bpermute_b32 v92, v82, v83
	s_waitcnt vmcnt(1)
	v_pk_add_f32 v[122:123], v[80:81], v[86:87]
	v_pk_add_f32 v[124:125], v[78:79], v[84:85]
	s_waitcnt vmcnt(0)
	v_pk_add_f32 v[90:91], v[76:77], v[90:91]
	v_pk_add_f32 v[88:89], v[74:75], v[88:89]
	v_cvt_pk_bf16_f32 v74, v124, v125
	v_cvt_pk_bf16_f32 v75, v122, v123
	v_mul_f32_e32 v93, v125, v125
	v_cvt_pk_bf16_f32 v76, v88, v89
	v_cvt_pk_bf16_f32 v77, v90, v91
	global_store_dwordx4 v[170:171], v[74:77], off sc1
	global_load_dwordx4 v[78:81], v[174:175], off offset:528
	global_load_dwordx4 v[84:87], v[174:175], off offset:512
	v_mul_f32_e32 v75, v119, v119
	v_mul_f32_e32 v76, v121, v121
	v_mul_f32_e32 v77, v115, v115
	v_mul_f32_e32 v115, v117, v117
	v_fmac_f32_e32 v75, v118, v118
	v_fmac_f32_e32 v76, v120, v120
	v_fmac_f32_e32 v77, v114, v114
	v_fmac_f32_e32 v115, v116, v116
	v_add_f32_e32 v75, v75, v76
	v_add_f32_e32 v76, v77, v115
	v_add_f32_e32 v74, v126, v127
	v_add_f32_e32 v75, v75, v76
	v_add_f32_e32 v75, v74, v75
	v_mul_f32_e32 v74, v111, v111
	v_mul_f32_e32 v77, v113, v113
	v_fmac_f32_e32 v74, v110, v110
	v_fmac_f32_e32 v77, v112, v112
	v_add_f32_e32 v74, v74, v77
	v_add_f32_e32 v77, v107, v109
	v_add_f32_e32 v74, v74, v77
	v_mul_f32_e32 v77, v163, v163
	v_mul_f32_e32 v107, v167, v167
	v_mul_f32_e32 v94, v123, v123
	v_mul_f32_e32 v89, v89, v89
	v_mul_f32_e32 v91, v91, v91
	v_fmac_f32_e32 v77, v162, v162
	v_fmac_f32_e32 v107, v166, v166
	v_fmac_f32_e32 v93, v124, v124
	v_fmac_f32_e32 v94, v122, v122
	v_fmac_f32_e32 v89, v88, v88
	v_fmac_f32_e32 v91, v90, v90
	v_add_f32_e32 v77, v77, v106
	v_add_f32_e32 v106, v107, v108
	v_add_f32_e32 v88, v93, v94
	v_add_f32_e32 v89, v89, v91
	v_add_f32_e32 v77, v77, v106
	v_add_f32_e32 v88, v88, v89
	v_add_f32_e32 v106, v74, v77
	ds_bpermute_b32 v76, v82, v75
	ds_bpermute_b32 v107, v82, v106
	v_cndmask_b32_e32 v74, v161, v149, vcc
	v_lshlrev_b32_e32 v74, 2, v74
	v_cmp_lt_i32_e32 vcc, 0, v154
	s_waitcnt lgkmcnt(1)
	v_add_f32_e32 v76, v75, v76
	s_waitcnt lgkmcnt(0)
	v_add_f32_e32 v75, v106, v107
	ds_bpermute_b32 v77, v74, v76
	s_waitcnt vmcnt(0)
	v_pk_add_f32 v[72:73], v[72:73], v[86:87]
	v_pk_add_f32 v[70:71], v[70:71], v[84:85]
	v_pk_add_f32 v[84:85], v[68:69], v[80:81]
	v_pk_add_f32 v[80:81], v[66:67], v[78:79]
	v_mul_f32_e32 v66, v71, v71
	v_mul_f32_e32 v67, v73, v73
	v_mul_f32_e32 v68, v81, v81
	v_mul_f32_e32 v69, v85, v85
	v_fmac_f32_e32 v66, v70, v70
	v_fmac_f32_e32 v67, v72, v72
	v_fmac_f32_e32 v68, v80, v80
	v_fmac_f32_e32 v69, v84, v84
	v_add_f32_e32 v66, v66, v67
	v_add_f32_e32 v67, v68, v69
	v_add_f32_e32 v66, v66, v67
	v_add_f32_e32 v68, v88, v66
	ds_bpermute_b32 v79, v82, v68
	v_add_f32_e32 v67, v83, v92
	v_cvt_pk_bf16_f32 v78, v70, v71
	ds_bpermute_b32 v66, v74, v75
	ds_bpermute_b32 v69, v74, v67
	s_waitcnt lgkmcnt(2)
	v_add_f32_e32 v70, v68, v79
	ds_bpermute_b32 v71, v74, v70
	v_cvt_pk_bf16_f32 v79, v72, v73
	v_cvt_pk_bf16_f32 v80, v80, v81
	v_cvt_pk_bf16_f32 v81, v84, v85
	global_store_dwordx4 v[170:171], v[78:81], off offset:256 sc1
	s_and_saveexec_b64 s[38:39], vcc
	s_xor_b64 s[38:39], exec, s[38:39]
	s_cbranch_execz .LBB0_463
	v_cmp_ne_u32_e32 vcc, 1, v154
	s_and_saveexec_b64 s[40:41], vcc
	s_xor_b64 s[40:41], exec, s[40:41]
	s_cbranch_execz .LBB0_460
	s_waitcnt lgkmcnt(0)
	v_add_f32_e32 v66, v70, v71
	v_add_f32_e32 v67, v67, v69
	v_cndmask_b32_e64 v68, v66, v67, s[4:5]

.LBB0_463:
	s_andn2_saveexec_b64 s[38:39], s[38:39]
	v_add_f32_e32 v68, v76, v77
	s_or_b64 exec, exec, s[38:39]
	s_lshl_b32 s27, s37, 2
	s_or_b32 s38, s27, s59
	s_ashr_i32 s39, s38, 31
	s_ashr_i32 s37, s36, 31
	s_lshl_b64 s[38:39], s[38:39], 15
	s_add_u32 s27, s57, s38
	s_addc_u32 s29, s58, s39
	s_lshl_b64 s[36:37], s[36:37], 2
	s_add_u32 s27, s27, s36
	s_addc_u32 s29, s29, s37
	s_add_u32 s36, s27, s16
	s_addc_u32 s37, s29, s17
	s_waitcnt lgkmcnt(2)
	v_lshl_add_u64 v[66:67], s[36:37], 0, v[138:139]
	v_mov_b32_e32 v149, v139
	v_lshl_add_u64 v[66:67], v[66:67], 0, v[148:149]
	global_store_dword v[66:67], v68, off
	s_waitcnt lgkmcnt(1)
	v_lshlrev_b64 v[68:69], 12, v[152:153]
	v_lshl_add_u64 v[68:69], v[68:69], 0, v[150:151]
	v_lshl_add_u64 v[80:81], v[68:69], 0, s[18:19]
	v_lshl_add_u64 v[84:85], v[80:81], 2, s[0:1]
	s_waitcnt lgkmcnt(0)
	global_load_dwordx4 v[70:73], v[84:85], off
	global_load_dwordx4 v[76:79], v[84:85], off offset:16
	v_lshl_add_u64 v[80:81], v[80:81], 1, s[10:11]
	v_cmp_lt_i32_e32 vcc, 0, v154
	s_waitcnt vmcnt(1)
	v_pk_add_f32 v[64:65], v[64:65], v[72:73]
	v_pk_add_f32 v[62:63], v[62:63], v[70:71]
	s_waitcnt vmcnt(0)
	v_pk_add_f32 v[60:61], v[60:61], v[78:79]
	v_pk_add_f32 v[58:59], v[58:59], v[76:77]
	v_cvt_pk_bf16_f32 v70, v62, v63
	v_cvt_pk_bf16_f32 v71, v64, v65
	v_mul_f32_e32 v63, v63, v63
	v_cvt_pk_bf16_f32 v72, v58, v59
	v_cvt_pk_bf16_f32 v73, v60, v61
	global_store_dwordx4 v[80:81], v[70:73], off sc1
	global_load_dwordx4 v[70:73], v[84:85], off offset:512
	s_nop 0
	global_load_dwordx4 v[76:79], v[84:85], off offset:528
	v_lshl_add_u64 v[84:85], v[68:69], 0, s[20:21]
	v_lshl_add_u64 v[86:87], v[84:85], 2, s[0:1]
	v_mul_f32_e32 v75, v59, v59
	v_fmac_f32_e32 v75, v58, v58
	v_mul_f32_e32 v65, v65, v65
	v_fmac_f32_e32 v63, v62, v62
	v_fmac_f32_e32 v65, v64, v64
	v_add_f32_e32 v62, v63, v65
	s_waitcnt vmcnt(1)
	v_pk_add_f32 v[56:57], v[56:57], v[72:73]
	v_pk_add_f32 v[54:55], v[54:55], v[70:71]
	s_waitcnt vmcnt(0)
	v_pk_add_f32 v[52:53], v[52:53], v[78:79]
	v_pk_add_f32 v[50:51], v[50:51], v[76:77]
	v_cvt_pk_bf16_f32 v70, v54, v55
	v_cvt_pk_bf16_f32 v71, v56, v57
	s_nop 0
	v_cvt_pk_bf16_f32 v72, v50, v51
	v_cvt_pk_bf16_f32 v73, v52, v53
	global_store_dwordx4 v[80:81], v[70:73], off offset:256 sc1
	global_load_dwordx4 v[70:73], v[86:87], off
	s_nop 0
	global_load_dwordx4 v[76:79], v[86:87], off offset:16
	v_lshl_add_u64 v[80:81], v[84:85], 1, s[10:11]
	v_lshl_add_u64 v[84:85], v[68:69], 0, s[22:23]
	v_lshl_add_u64 v[68:69], v[68:69], 0, s[24:25]
	s_waitcnt vmcnt(1)
	v_pk_add_f32 v[48:49], v[48:49], v[72:73]
	v_pk_add_f32 v[46:47], v[46:47], v[70:71]
	s_waitcnt vmcnt(0)
	v_pk_add_f32 v[44:45], v[44:45], v[78:79]
	v_pk_add_f32 v[42:43], v[42:43], v[76:77]
	v_cvt_pk_bf16_f32 v70, v46, v47
	v_cvt_pk_bf16_f32 v71, v48, v49
	s_nop 0
	v_cvt_pk_bf16_f32 v72, v42, v43
	v_cvt_pk_bf16_f32 v73, v44, v45
	global_store_dwordx4 v[80:81], v[70:73], off sc1
	global_load_dwordx4 v[70:73], v[86:87], off offset:512
	s_nop 0
	global_load_dwordx4 v[76:79], v[86:87], off offset:528
	v_lshl_add_u64 v[86:87], v[84:85], 2, s[0:1]
	v_mul_f32_e32 v43, v43, v43
	v_mul_f32_e32 v45, v45, v45
	v_fmac_f32_e32 v43, v42, v42
	v_fmac_f32_e32 v45, v44, v44
	s_waitcnt vmcnt(1)
	v_pk_add_f32 v[72:73], v[40:41], v[72:73]
	v_pk_add_f32 v[70:71], v[38:39], v[70:71]
	s_waitcnt vmcnt(0)
	v_pk_add_f32 v[78:79], v[36:37], v[78:79]
	v_pk_add_f32 v[76:77], v[34:35], v[76:77]
	v_cvt_pk_bf16_f32 v34, v70, v71
	v_cvt_pk_bf16_f32 v35, v72, v73
	v_mul_f32_e32 v42, v73, v73
	v_cvt_pk_bf16_f32 v36, v76, v77
	v_cvt_pk_bf16_f32 v37, v78, v79
	global_store_dwordx4 v[80:81], v[34:37], off offset:256 sc1
	global_load_dwordx4 v[34:37], v[86:87], off
	s_nop 0
	global_load_dwordx4 v[38:41], v[86:87], off offset:16
	v_lshl_add_u64 v[80:81], v[84:85], 1, s[10:11]
	v_lshl_add_u64 v[84:85], v[68:69], 2, s[0:1]
	v_lshl_add_u64 v[68:69], v[68:69], 1, s[10:11]
	v_mul_f32_e32 v44, v79, v79
	v_fmac_f32_e32 v42, v72, v72
	v_fmac_f32_e32 v44, v78, v78
	s_waitcnt vmcnt(1)
	v_pk_add_f32 v[36:37], v[32:33], v[36:37]
	v_pk_add_f32 v[34:35], v[30:31], v[34:35]
	s_waitcnt vmcnt(0)
	v_pk_add_f32 v[40:41], v[28:29], v[40:41]
	v_pk_add_f32 v[38:39], v[26:27], v[38:39]
	v_cvt_pk_bf16_f32 v26, v34, v35
	v_cvt_pk_bf16_f32 v27, v36, v37
	s_nop 0
	v_cvt_pk_bf16_f32 v28, v38, v39
	v_cvt_pk_bf16_f32 v29, v40, v41
	global_store_dwordx4 v[80:81], v[26:29], off sc1
	global_load_dwordx4 v[26:29], v[86:87], off offset:512
	s_nop 0
	global_load_dwordx4 v[30:33], v[86:87], off offset:528
	s_waitcnt vmcnt(1)
	v_pk_add_f32 v[28:29], v[24:25], v[28:29]
	v_pk_add_f32 v[26:27], v[22:23], v[26:27]
	s_waitcnt vmcnt(0)
	v_pk_add_f32 v[32:33], v[20:21], v[32:33]
	v_pk_add_f32 v[30:31], v[18:19], v[30:31]
	v_cvt_pk_bf16_f32 v18, v26, v27
	v_cvt_pk_bf16_f32 v19, v28, v29
	v_mul_f32_e32 v27, v27, v27
	v_cvt_pk_bf16_f32 v20, v30, v31
	v_cvt_pk_bf16_f32 v21, v32, v33
	global_store_dwordx4 v[80:81], v[18:21], off offset:256 sc1
	global_load_dwordx4 v[18:21], v[84:85], off
	s_nop 0
	global_load_dwordx4 v[22:25], v[84:85], off offset:16
	v_mul_f32_e32 v80, v61, v61
	v_fmac_f32_e32 v80, v60, v60
	v_mul_f32_e32 v29, v29, v29
	v_mul_f32_e32 v31, v31, v31
	v_mul_f32_e32 v33, v33, v33
	v_fmac_f32_e32 v27, v26, v26
	v_fmac_f32_e32 v29, v28, v28
	v_fmac_f32_e32 v31, v30, v30
	v_fmac_f32_e32 v33, v32, v32
	v_add_f32_e32 v26, v27, v29
	v_add_f32_e32 v27, v31, v33
	v_add_f32_e32 v26, v26, v27
	s_waitcnt vmcnt(1)
	v_pk_add_f32 v[58:59], v[16:17], v[20:21]
	v_pk_add_f32 v[60:61], v[14:15], v[18:19]
	s_waitcnt vmcnt(0)
	v_pk_add_f32 v[24:25], v[12:13], v[24:25]
	v_pk_add_f32 v[22:23], v[10:11], v[22:23]
	v_cvt_pk_bf16_f32 v10, v60, v61
	v_cvt_pk_bf16_f32 v11, v58, v59
	v_mul_f32_e32 v27, v61, v61
	v_cvt_pk_bf16_f32 v12, v22, v23
	v_cvt_pk_bf16_f32 v13, v24, v25
	global_store_dwordx4 v[68:69], v[10:13], off sc1
	global_load_dwordx4 v[14:17], v[84:85], off offset:528
	global_load_dwordx4 v[18:21], v[84:85], off offset:512
	v_mul_f32_e32 v11, v55, v55
	v_mul_f32_e32 v12, v57, v57
	v_mul_f32_e32 v13, v51, v51
	v_mul_f32_e32 v51, v53, v53
	v_fmac_f32_e32 v11, v54, v54
	v_fmac_f32_e32 v12, v56, v56
	v_fmac_f32_e32 v13, v50, v50
	v_fmac_f32_e32 v51, v52, v52
	v_add_f32_e32 v11, v11, v12
	v_add_f32_e32 v12, v13, v51
	v_add_f32_e32 v11, v11, v12
	v_mul_f32_e32 v12, v47, v47
	v_mul_f32_e32 v13, v49, v49
	v_fmac_f32_e32 v12, v46, v46
	v_fmac_f32_e32 v13, v48, v48
	v_add_f32_e32 v12, v12, v13
	v_add_f32_e32 v13, v43, v45
	v_add_f32_e32 v12, v12, v13
	v_mul_f32_e32 v13, v71, v71
	v_mul_f32_e32 v43, v77, v77
	v_fmac_f32_e32 v13, v70, v70
	v_fmac_f32_e32 v43, v76, v76
	v_add_f32_e32 v10, v75, v80
	v_add_f32_e32 v13, v13, v42
	v_add_f32_e32 v42, v43, v44
	v_add_f32_e32 v10, v62, v10
	v_add_f32_e32 v13, v13, v42
	v_add_f32_e32 v10, v10, v11
	v_add_f32_e32 v13, v12, v13
	ds_bpermute_b32 v11, v82, v10
	ds_bpermute_b32 v42, v82, v13
	v_mul_f32_e32 v28, v59, v59
	v_mul_f32_e32 v23, v23, v23
	v_mul_f32_e32 v25, v25, v25
	s_waitcnt lgkmcnt(1)
	v_add_f32_e32 v11, v10, v11
	s_waitcnt lgkmcnt(0)
	v_add_f32_e32 v10, v13, v42
	v_mul_f32_e32 v13, v35, v35
	v_mul_f32_e32 v35, v37, v37
	v_mul_f32_e32 v37, v39, v39
	v_mul_f32_e32 v39, v41, v41
	v_fmac_f32_e32 v13, v34, v34
	v_fmac_f32_e32 v35, v36, v36
	v_fmac_f32_e32 v37, v38, v38
	v_fmac_f32_e32 v39, v40, v40
	v_fmac_f32_e32 v27, v60, v60
	v_fmac_f32_e32 v28, v58, v58
	v_fmac_f32_e32 v23, v22, v22
	v_fmac_f32_e32 v25, v24, v24
	v_add_f32_e32 v13, v13, v35
	v_add_f32_e32 v34, v37, v39
	v_add_f32_e32 v22, v27, v28
	v_add_f32_e32 v23, v23, v25
	v_add_f32_e32 v13, v13, v34
	v_add_f32_e32 v22, v22, v23
	v_add_f32_e32 v13, v13, v26
	ds_bpermute_b32 v26, v82, v13
	ds_bpermute_b32 v12, v74, v11
	s_waitcnt vmcnt(0)
	v_pk_add_f32 v[8:9], v[8:9], v[20:21]
	v_pk_add_f32 v[6:7], v[6:7], v[18:19]
	v_pk_add_f32 v[18:19], v[4:5], v[16:17]
	v_pk_add_f32 v[16:17], v[2:3], v[14:15]
	v_mul_f32_e32 v2, v7, v7
	v_mul_f32_e32 v3, v9, v9
	v_mul_f32_e32 v4, v17, v17
	v_mul_f32_e32 v5, v19, v19
	v_fmac_f32_e32 v2, v6, v6
	v_fmac_f32_e32 v3, v8, v8
	v_fmac_f32_e32 v4, v16, v16
	v_fmac_f32_e32 v5, v18, v18
	v_add_f32_e32 v2, v2, v3
	v_add_f32_e32 v3, v4, v5
	v_add_f32_e32 v2, v2, v3
	v_add_f32_e32 v2, v22, v2
	ds_bpermute_b32 v15, v82, v2
	s_waitcnt lgkmcnt(2)
	v_add_f32_e32 v4, v13, v26
	v_cvt_pk_bf16_f32 v14, v6, v7
	ds_bpermute_b32 v3, v74, v10
	ds_bpermute_b32 v5, v74, v4
	s_waitcnt lgkmcnt(2)
	v_add_f32_e32 v6, v2, v15
	ds_bpermute_b32 v7, v74, v6
	v_cvt_pk_bf16_f32 v15, v8, v9
	v_cvt_pk_bf16_f32 v16, v16, v17
	v_cvt_pk_bf16_f32 v17, v18, v19
	global_store_dwordx4 v[68:69], v[14:17], off offset:256 sc1
	s_and_saveexec_b64 s[36:37], vcc
	s_xor_b64 s[36:37], exec, s[36:37]
	s_cbranch_execz .LBB0_471
	v_cmp_ne_u32_e32 vcc, 1, v154
	s_and_saveexec_b64 s[38:39], vcc
	s_xor_b64 s[38:39], exec, s[38:39]
	s_cbranch_execz .LBB0_468
	s_waitcnt lgkmcnt(0)
	v_add_f32_e32 v2, v6, v7
	v_add_f32_e32 v3, v4, v5
	v_cndmask_b32_e64 v2, v2, v3, s[4:5]

.LBB0_530:
	v_lshl_or_b32 v136, s11, 8, v152
	v_lshl_add_u32 v152, v151, 2, s76
	v_or_b32_e32 v140, s41, v136
	ds_read_b32 v136, v152
	s_lshl_b32 s6, s15, 8
	v_add_u32_e32 v138, s6, v151
	v_ashrrev_i32_e32 v139, 31, v138
	v_ashrrev_i32_e32 v141, 31, v140
	v_lshlrev_b64 v[142:143], 11, v[138:139]
	v_lshl_add_u64 v[142:143], s[2:3], 0, v[142:143]
	v_lshlrev_b64 v[140:141], 1, v[140:141]
	v_lshl_add_u64 v[142:143], v[142:143], 0, v[140:141]
	s_waitcnt lgkmcnt(0)
	v_pk_mul_f32 v[128:129], v[128:129], v[136:137] op_sel_hi:[1,0]
	v_pk_mul_f32 v[126:127], v[126:127], v[136:137] op_sel_hi:[1,0]
	v_pk_mul_f32 v[144:145], v[124:125], v[136:137] op_sel_hi:[1,0]
	v_pk_mul_f32 v[124:125], v[122:123], v[136:137] op_sel_hi:[1,0]
	v_cvt_pk_bf16_f32 v122, v126, v127
	v_cvt_pk_bf16_f32 v123, v128, v129
	v_or_b32_e32 v153, 16, v151
	v_cvt_pk_bf16_f32 v124, v124, v125
	v_cvt_pk_bf16_f32 v125, v144, v145
	global_store_dwordx4 v[142:143], v[122:125], off sc1
	v_pk_mul_f32 v[118:119], v[118:119], v[136:137] op_sel_hi:[1,0]
	v_pk_mul_f32 v[120:121], v[120:121], v[136:137] op_sel_hi:[1,0]
	v_pk_mul_f32 v[122:123], v[116:117], v[136:137] op_sel_hi:[1,0]
	v_pk_mul_f32 v[116:117], v[114:115], v[136:137] op_sel_hi:[1,0]
	v_cvt_pk_bf16_f32 v114, v118, v119
	v_cvt_pk_bf16_f32 v115, v120, v121
	v_or_b32_e32 v147, 32, v151
	v_cvt_pk_bf16_f32 v116, v116, v117
	v_cvt_pk_bf16_f32 v117, v122, v123
	global_store_dwordx4 v[142:143], v[114:117], off offset:256 sc1
	v_or_b32_e32 v146, 48, v151
	s_add_i32 s35, s35, 1
	v_lshl_add_u32 v114, v153, 2, s76
	ds_read_b32 v114, v114
	v_add_u32_e32 v116, s6, v153
	v_ashrrev_i32_e32 v117, 31, v116
	v_lshlrev_b64 v[116:117], 11, v[116:117]
	v_lshl_add_u64 v[116:117], s[2:3], 0, v[116:117]
	v_lshl_add_u64 v[116:117], v[116:117], 0, v[140:141]
	s_waitcnt lgkmcnt(0)
	v_pk_mul_f32 v[112:113], v[112:113], v[114:115] op_sel_hi:[1,0]
	v_pk_mul_f32 v[110:111], v[110:111], v[114:115] op_sel_hi:[1,0]
	v_pk_mul_f32 v[118:119], v[108:109], v[114:115] op_sel_hi:[1,0]
	v_pk_mul_f32 v[108:109], v[106:107], v[114:115] op_sel_hi:[1,0]
	v_cvt_pk_bf16_f32 v106, v110, v111
	v_cvt_pk_bf16_f32 v107, v112, v113
	v_pk_mul_f32 v[102:103], v[102:103], v[114:115] op_sel_hi:[1,0]
	v_cvt_pk_bf16_f32 v108, v108, v109
	v_cvt_pk_bf16_f32 v109, v118, v119
	global_store_dwordx4 v[116:117], v[106:109], off sc1
	v_pk_mul_f32 v[104:105], v[104:105], v[114:115] op_sel_hi:[1,0]
	s_nop 0
	v_pk_mul_f32 v[106:107], v[100:101], v[114:115] op_sel_hi:[1,0]
	v_pk_mul_f32 v[100:101], v[98:99], v[114:115] op_sel_hi:[1,0]
	v_cvt_pk_bf16_f32 v98, v102, v103
	v_cvt_pk_bf16_f32 v99, v104, v105
	s_nop 0
	v_cvt_pk_bf16_f32 v100, v100, v101
	v_cvt_pk_bf16_f32 v101, v106, v107
	global_store_dwordx4 v[116:117], v[98:101], off offset:256 sc1
	s_nop 1
	v_lshl_add_u32 v98, v147, 2, s76
	ds_read_b32 v98, v98
	v_add_u32_e32 v100, s6, v147
	v_ashrrev_i32_e32 v101, 31, v100
	v_lshlrev_b64 v[100:101], 11, v[100:101]
	v_lshl_add_u64 v[100:101], s[2:3], 0, v[100:101]
	v_lshl_add_u64 v[100:101], v[100:101], 0, v[140:141]
	s_waitcnt lgkmcnt(0)
	v_pk_mul_f32 v[96:97], v[96:97], v[98:99] op_sel_hi:[1,0]
	v_pk_mul_f32 v[94:95], v[94:95], v[98:99] op_sel_hi:[1,0]
	v_pk_mul_f32 v[102:103], v[92:93], v[98:99] op_sel_hi:[1,0]
	v_pk_mul_f32 v[92:93], v[90:91], v[98:99] op_sel_hi:[1,0]
	v_cvt_pk_bf16_f32 v90, v94, v95
	v_cvt_pk_bf16_f32 v91, v96, v97
	v_pk_mul_f32 v[86:87], v[86:87], v[98:99] op_sel_hi:[1,0]
	v_cvt_pk_bf16_f32 v92, v92, v93
	v_cvt_pk_bf16_f32 v93, v102, v103
	global_store_dwordx4 v[100:101], v[90:93], off sc1
	v_pk_mul_f32 v[88:89], v[88:89], v[98:99] op_sel_hi:[1,0]
	s_nop 0
	v_pk_mul_f32 v[90:91], v[84:85], v[98:99] op_sel_hi:[1,0]
	v_pk_mul_f32 v[84:85], v[82:83], v[98:99] op_sel_hi:[1,0]
	v_cvt_pk_bf16_f32 v82, v86, v87
	v_cvt_pk_bf16_f32 v83, v88, v89
	s_nop 0
	v_cvt_pk_bf16_f32 v84, v84, v85
	v_cvt_pk_bf16_f32 v85, v90, v91
	global_store_dwordx4 v[100:101], v[82:85], off offset:256 sc1
	s_nop 1
	v_lshl_add_u32 v82, v146, 2, s76
	ds_read_b32 v82, v82
	v_add_u32_e32 v84, s6, v146
	v_ashrrev_i32_e32 v85, 31, v84
	v_lshlrev_b64 v[84:85], 11, v[84:85]
	v_lshl_add_u64 v[84:85], s[2:3], 0, v[84:85]
	v_lshl_add_u64 v[84:85], v[84:85], 0, v[140:141]
	s_waitcnt lgkmcnt(0)
	v_pk_mul_f32 v[80:81], v[80:81], v[82:83] op_sel_hi:[1,0]
	v_pk_mul_f32 v[78:79], v[78:79], v[82:83] op_sel_hi:[1,0]
	v_pk_mul_f32 v[86:87], v[76:77], v[82:83] op_sel_hi:[1,0]
	v_pk_mul_f32 v[76:77], v[74:75], v[82:83] op_sel_hi:[1,0]
	v_cvt_pk_bf16_f32 v74, v78, v79
	v_cvt_pk_bf16_f32 v75, v80, v81
	v_pk_mul_f32 v[70:71], v[70:71], v[82:83] op_sel_hi:[1,0]
	v_cvt_pk_bf16_f32 v76, v76, v77
	v_cvt_pk_bf16_f32 v77, v86, v87
	global_store_dwordx4 v[84:85], v[74:77], off sc1
	v_pk_mul_f32 v[72:73], v[72:73], v[82:83] op_sel_hi:[1,0]
	s_mov_b64 s[6:7], 0
	v_pk_mul_f32 v[74:75], v[68:69], v[82:83] op_sel_hi:[1,0]
	v_pk_mul_f32 v[68:69], v[66:67], v[82:83] op_sel_hi:[1,0]
	v_cvt_pk_bf16_f32 v66, v70, v71
	v_cvt_pk_bf16_f32 v67, v72, v73
	s_nop 0
	v_cvt_pk_bf16_f32 v68, v68, v69
	v_cvt_pk_bf16_f32 v69, v74, v75
	global_store_dwordx4 v[84:85], v[66:69], off offset:256 sc1
	ds_read_b32 v66, v152 offset:512
	s_waitcnt lgkmcnt(0)
	v_pk_mul_f32 v[64:65], v[64:65], v[66:67] op_sel_hi:[1,0]
	v_add_u32_e32 v68, 0x80, v138
	v_ashrrev_i32_e32 v69, 31, v68
	v_lshlrev_b64 v[68:69], 11, v[68:69]
	v_lshl_add_u64 v[68:69], s[2:3], 0, v[68:69]
	v_lshl_add_u64 v[68:69], v[68:69], 0, v[140:141]
	v_pk_mul_f32 v[62:63], v[62:63], v[66:67] op_sel_hi:[1,0]
	v_pk_mul_f32 v[70:71], v[60:61], v[66:67] op_sel_hi:[1,0]
	v_pk_mul_f32 v[60:61], v[58:59], v[66:67] op_sel_hi:[1,0]
	v_cvt_pk_bf16_f32 v58, v62, v63
	v_cvt_pk_bf16_f32 v59, v64, v65
	v_pk_mul_f32 v[54:55], v[54:55], v[66:67] op_sel_hi:[1,0]
	v_cvt_pk_bf16_f32 v60, v60, v61
	v_cvt_pk_bf16_f32 v61, v70, v71
	global_store_dwordx4 v[68:69], v[58:61], off sc1
	v_pk_mul_f32 v[56:57], v[56:57], v[66:67] op_sel_hi:[1,0]
	s_nop 0
	v_pk_mul_f32 v[58:59], v[52:53], v[66:67] op_sel_hi:[1,0]
	v_pk_mul_f32 v[52:53], v[50:51], v[66:67] op_sel_hi:[1,0]
	v_cvt_pk_bf16_f32 v50, v54, v55
	v_cvt_pk_bf16_f32 v51, v56, v57
	s_nop 0
	v_cvt_pk_bf16_f32 v52, v52, v53
	v_cvt_pk_bf16_f32 v53, v58, v59
	global_store_dwordx4 v[68:69], v[50:53], off offset:256 sc1
	ds_read_b32 v50, v152 offset:576
	s_waitcnt lgkmcnt(0)
	v_pk_mul_f32 v[48:49], v[48:49], v[50:51] op_sel_hi:[1,0]
	v_add_u32_e32 v52, 0x90, v138
	v_ashrrev_i32_e32 v53, 31, v52
	v_lshlrev_b64 v[52:53], 11, v[52:53]
	v_lshl_add_u64 v[52:53], s[2:3], 0, v[52:53]
	v_lshl_add_u64 v[52:53], v[52:53], 0, v[140:141]
	v_pk_mul_f32 v[46:47], v[46:47], v[50:51] op_sel_hi:[1,0]
	v_pk_mul_f32 v[54:55], v[44:45], v[50:51] op_sel_hi:[1,0]
	v_pk_mul_f32 v[44:45], v[42:43], v[50:51] op_sel_hi:[1,0]
	v_cvt_pk_bf16_f32 v42, v46, v47
	v_cvt_pk_bf16_f32 v43, v48, v49
	v_pk_mul_f32 v[38:39], v[38:39], v[50:51] op_sel_hi:[1,0]
	v_cvt_pk_bf16_f32 v44, v44, v45
	v_cvt_pk_bf16_f32 v45, v54, v55
	global_store_dwordx4 v[52:53], v[42:45], off sc1
	v_pk_mul_f32 v[40:41], v[40:41], v[50:51] op_sel_hi:[1,0]
	s_nop 0
	v_pk_mul_f32 v[42:43], v[36:37], v[50:51] op_sel_hi:[1,0]
	v_pk_mul_f32 v[36:37], v[34:35], v[50:51] op_sel_hi:[1,0]
	v_cvt_pk_bf16_f32 v34, v38, v39
	v_cvt_pk_bf16_f32 v35, v40, v41
	s_nop 0
	v_cvt_pk_bf16_f32 v36, v36, v37
	v_cvt_pk_bf16_f32 v37, v42, v43
	global_store_dwordx4 v[52:53], v[34:37], off offset:256 sc1
	ds_read_b32 v34, v152 offset:640
	s_waitcnt lgkmcnt(0)
	v_pk_mul_f32 v[32:33], v[32:33], v[34:35] op_sel_hi:[1,0]
	v_add_u32_e32 v36, 0xa0, v138
	v_ashrrev_i32_e32 v37, 31, v36
	v_lshlrev_b64 v[36:37], 11, v[36:37]
	v_lshl_add_u64 v[36:37], s[2:3], 0, v[36:37]
	v_lshl_add_u64 v[36:37], v[36:37], 0, v[140:141]
	v_pk_mul_f32 v[30:31], v[30:31], v[34:35] op_sel_hi:[1,0]
	v_pk_mul_f32 v[38:39], v[28:29], v[34:35] op_sel_hi:[1,0]
	v_pk_mul_f32 v[28:29], v[26:27], v[34:35] op_sel_hi:[1,0]
	v_cvt_pk_bf16_f32 v26, v30, v31
	v_cvt_pk_bf16_f32 v27, v32, v33
	v_pk_mul_f32 v[22:23], v[22:23], v[34:35] op_sel_hi:[1,0]
	v_cvt_pk_bf16_f32 v28, v28, v29
	v_cvt_pk_bf16_f32 v29, v38, v39
	global_store_dwordx4 v[36:37], v[26:29], off sc1
	v_pk_mul_f32 v[24:25], v[24:25], v[34:35] op_sel_hi:[1,0]
	s_nop 0
	v_pk_mul_f32 v[26:27], v[20:21], v[34:35] op_sel_hi:[1,0]
	v_pk_mul_f32 v[20:21], v[18:19], v[34:35] op_sel_hi:[1,0]
	v_cvt_pk_bf16_f32 v18, v22, v23
	v_cvt_pk_bf16_f32 v19, v24, v25
	s_nop 0
	v_cvt_pk_bf16_f32 v20, v20, v21
	v_cvt_pk_bf16_f32 v21, v26, v27
	global_store_dwordx4 v[36:37], v[18:21], off offset:256 sc1
	ds_read_b32 v18, v152 offset:704
	s_waitcnt lgkmcnt(0)
	v_pk_mul_f32 v[16:17], v[16:17], v[18:19] op_sel_hi:[1,0]
	v_add_u32_e32 v20, 0xb0, v138
	v_ashrrev_i32_e32 v21, 31, v20
	v_lshlrev_b64 v[20:21], 11, v[20:21]
	v_lshl_add_u64 v[20:21], s[2:3], 0, v[20:21]
	v_lshl_add_u64 v[20:21], v[20:21], 0, v[140:141]
	v_pk_mul_f32 v[14:15], v[14:15], v[18:19] op_sel_hi:[1,0]
	v_pk_mul_f32 v[22:23], v[12:13], v[18:19] op_sel_hi:[1,0]
	v_pk_mul_f32 v[12:13], v[10:11], v[18:19] op_sel_hi:[1,0]
	v_cvt_pk_bf16_f32 v10, v14, v15
	v_cvt_pk_bf16_f32 v11, v16, v17
	v_pk_mul_f32 v[8:9], v[8:9], v[18:19] op_sel_hi:[1,0]
	v_cvt_pk_bf16_f32 v12, v12, v13
	v_cvt_pk_bf16_f32 v13, v22, v23
	global_store_dwordx4 v[20:21], v[10:13], off sc1
	v_pk_mul_f32 v[6:7], v[6:7], v[18:19] op_sel_hi:[1,0]
	s_nop 0
	v_pk_mul_f32 v[10:11], v[4:5], v[18:19] op_sel_hi:[1,0]
	v_pk_mul_f32 v[4:5], v[2:3], v[18:19] op_sel_hi:[1,0]
	v_cvt_pk_bf16_f32 v2, v6, v7
	v_cvt_pk_bf16_f32 v3, v8, v9
	s_nop 0
	v_cvt_pk_bf16_f32 v4, v4, v5
	v_cvt_pk_bf16_f32 v5, v10, v11
	global_store_dwordx4 v[20:21], v[2:5], off offset:256 sc1
	s_waitcnt vmcnt(0)
	s_barrier

.LBB0_567:
	v_lshl_add_u32 v144, s30, 8, v146
	v_lshl_or_b32 v142, s66, 8, v148
	v_ashrrev_i32_e32 v143, 31, v142
	v_ashrrev_i32_e32 v145, 31, v144
	v_lshl_add_u64 v[152:153], v[142:143], 1, s[4:5]
	v_lshlrev_b64 v[142:143], 11, v[144:145]
	v_lshl_add_u64 v[142:143], v[152:153], 0, v[142:143]
	v_pk_add_f32 v[128:129], v[128:129], 0 op_sel_hi:[1,0]
	v_pk_add_f32 v[126:127], v[126:127], 0 op_sel_hi:[1,0]
	v_pk_add_f32 v[154:155], v[124:125], 0 op_sel_hi:[1,0]
	v_pk_add_f32 v[124:125], v[122:123], 0 op_sel_hi:[1,0]
	v_cvt_pk_bf16_f32 v122, v126, v127
	v_cvt_pk_bf16_f32 v123, v128, v129
	v_pk_add_f32 v[118:119], v[118:119], 0 op_sel_hi:[1,0]
	v_cvt_pk_bf16_f32 v124, v124, v125
	v_cvt_pk_bf16_f32 v125, v154, v155
	global_store_dwordx4 v[142:143], v[122:125], off sc1
	v_pk_add_f32 v[120:121], v[120:121], 0 op_sel_hi:[1,0]
	v_pk_add_f32 v[114:115], v[114:115], 0 op_sel_hi:[1,0]
	v_pk_add_f32 v[122:123], v[112:113], 0 op_sel_hi:[1,0]
	v_pk_add_f32 v[112:113], v[110:111], 0 op_sel_hi:[1,0]
	v_cvt_pk_bf16_f32 v110, v118, v119
	v_cvt_pk_bf16_f32 v111, v120, v121
	v_pk_add_f32 v[102:103], v[102:103], 0 op_sel_hi:[1,0]
	v_cvt_pk_bf16_f32 v112, v112, v113
	v_cvt_pk_bf16_f32 v113, v122, v123
	global_store_dwordx4 v[142:143], v[110:113], off offset:256 sc1
	v_pk_add_f32 v[104:105], v[104:105], 0 op_sel_hi:[1,0]
	v_pk_add_f32 v[98:99], v[98:99], 0 op_sel_hi:[1,0]
	v_or_b32_e32 v110, 16, v144
	v_ashrrev_i32_e32 v111, 31, v110
	v_lshlrev_b64 v[110:111], 11, v[110:111]
	v_lshl_add_u64 v[110:111], v[152:153], 0, v[110:111]
	v_pk_add_f32 v[112:113], v[116:117], 0 op_sel_hi:[1,0]
	v_pk_add_f32 v[116:117], v[108:109], 0 op_sel_hi:[1,0]
	v_pk_add_f32 v[108:109], v[106:107], 0 op_sel_hi:[1,0]
	v_cvt_pk_bf16_f32 v106, v114, v115
	v_cvt_pk_bf16_f32 v107, v112, v113
	v_pk_add_f32 v[86:87], v[86:87], 0 op_sel_hi:[1,0]
	v_cvt_pk_bf16_f32 v108, v108, v109
	v_cvt_pk_bf16_f32 v109, v116, v117
	global_store_dwordx4 v[110:111], v[106:109], off sc1
	v_pk_add_f32 v[88:89], v[88:89], 0 op_sel_hi:[1,0]
	v_pk_add_f32 v[82:83], v[82:83], 0 op_sel_hi:[1,0]
	v_pk_add_f32 v[106:107], v[96:97], 0 op_sel_hi:[1,0]
	v_pk_add_f32 v[96:97], v[94:95], 0 op_sel_hi:[1,0]
	v_cvt_pk_bf16_f32 v94, v102, v103
	v_cvt_pk_bf16_f32 v95, v104, v105
	v_pk_add_f32 v[72:73], v[72:73], 0 op_sel_hi:[1,0]
	v_cvt_pk_bf16_f32 v96, v96, v97
	v_cvt_pk_bf16_f32 v97, v106, v107
	global_store_dwordx4 v[110:111], v[94:97], off offset:256 sc1
	v_pk_add_f32 v[70:71], v[70:71], 0 op_sel_hi:[1,0]
	v_pk_add_f32 v[62:63], v[62:63], 0 op_sel_hi:[1,0]
	v_or_b32_e32 v94, 32, v144
	v_ashrrev_i32_e32 v95, 31, v94
	v_lshlrev_b64 v[94:95], 11, v[94:95]
	v_lshl_add_u64 v[94:95], v[152:153], 0, v[94:95]
	v_pk_add_f32 v[96:97], v[100:101], 0 op_sel_hi:[1,0]
	v_pk_add_f32 v[100:101], v[92:93], 0 op_sel_hi:[1,0]
	v_pk_add_f32 v[92:93], v[90:91], 0 op_sel_hi:[1,0]
	v_cvt_pk_bf16_f32 v90, v98, v99
	v_cvt_pk_bf16_f32 v91, v96, v97
	v_pk_add_f32 v[64:65], v[64:65], 0 op_sel_hi:[1,0]
	v_cvt_pk_bf16_f32 v92, v92, v93
	v_cvt_pk_bf16_f32 v93, v100, v101
	global_store_dwordx4 v[94:95], v[90:93], off sc1
	v_pk_add_f32 v[56:57], v[56:57], 0 op_sel_hi:[1,0]
	v_pk_add_f32 v[54:55], v[54:55], 0 op_sel_hi:[1,0]
	v_pk_add_f32 v[90:91], v[80:81], 0 op_sel_hi:[1,0]
	v_pk_add_f32 v[80:81], v[78:79], 0 op_sel_hi:[1,0]
	v_cvt_pk_bf16_f32 v78, v86, v87
	v_cvt_pk_bf16_f32 v79, v88, v89
	v_pk_add_f32 v[50:51], v[50:51], 0 op_sel_hi:[1,0]
	v_cvt_pk_bf16_f32 v80, v80, v81
	v_cvt_pk_bf16_f32 v81, v90, v91
	global_store_dwordx4 v[94:95], v[78:81], off offset:256 sc1
	v_pk_add_f32 v[40:41], v[40:41], 0 op_sel_hi:[1,0]
	v_pk_add_f32 v[38:39], v[38:39], 0 op_sel_hi:[1,0]
	v_or_b32_e32 v78, 48, v144
	v_ashrrev_i32_e32 v79, 31, v78
	v_lshlrev_b64 v[78:79], 11, v[78:79]
	v_lshl_add_u64 v[78:79], v[152:153], 0, v[78:79]
	v_pk_add_f32 v[80:81], v[84:85], 0 op_sel_hi:[1,0]
	v_pk_add_f32 v[84:85], v[76:77], 0 op_sel_hi:[1,0]
	v_pk_add_f32 v[76:77], v[74:75], 0 op_sel_hi:[1,0]
	v_cvt_pk_bf16_f32 v74, v82, v83
	v_cvt_pk_bf16_f32 v75, v80, v81
	v_pk_add_f32 v[34:35], v[34:35], 0 op_sel_hi:[1,0]
	v_cvt_pk_bf16_f32 v76, v76, v77
	v_cvt_pk_bf16_f32 v77, v84, v85
	global_store_dwordx4 v[78:79], v[74:77], off sc1
	v_pk_add_f32 v[24:25], v[24:25], 0 op_sel_hi:[1,0]
	v_pk_add_f32 v[22:23], v[22:23], 0 op_sel_hi:[1,0]
	v_pk_add_f32 v[74:75], v[68:69], 0 op_sel_hi:[1,0]
	v_pk_add_f32 v[68:69], v[66:67], 0 op_sel_hi:[1,0]
	v_cvt_pk_bf16_f32 v66, v70, v71
	v_cvt_pk_bf16_f32 v67, v72, v73
	v_pk_add_f32 v[18:19], v[18:19], 0 op_sel_hi:[1,0]
	v_cvt_pk_bf16_f32 v68, v68, v69
	v_cvt_pk_bf16_f32 v69, v74, v75
	global_store_dwordx4 v[78:79], v[66:69], off offset:256 sc1
	v_pk_add_f32 v[8:9], v[8:9], 0 op_sel_hi:[1,0]
	v_pk_add_f32 v[6:7], v[6:7], 0 op_sel_hi:[1,0]
	v_pk_add_f32 v[68:69], v[60:61], 0 op_sel_hi:[1,0]
	v_pk_add_f32 v[60:61], v[58:59], 0 op_sel_hi:[1,0]
	v_cvt_pk_bf16_f32 v58, v62, v63
	v_add_co_u32_e32 v62, vcc, s61, v142
	v_cvt_pk_bf16_f32 v59, v64, v65
	v_cvt_pk_bf16_f32 v60, v60, v61
	v_cvt_pk_bf16_f32 v61, v68, v69
	v_lshl_add_u64 v[66:67], v[142:143], 0, s[12:13]
	s_nop 0
	v_addc_co_u32_e32 v63, vcc, 0, v143, vcc
	global_store_dwordx4 v[62:63], v[58:61], off sc1
	s_nop 1
	v_pk_add_f32 v[58:59], v[48:49], 0 op_sel_hi:[1,0]
	v_pk_add_f32 v[48:49], v[46:47], 0 op_sel_hi:[1,0]
	v_cvt_pk_bf16_f32 v46, v54, v55
	v_cvt_pk_bf16_f32 v47, v56, v57
	s_nop 0
	v_cvt_pk_bf16_f32 v48, v48, v49
	v_cvt_pk_bf16_f32 v49, v58, v59
	global_store_dwordx4 v[66:67], v[46:49], off offset:256 sc1
	s_nop 1
	v_pk_add_f32 v[48:49], v[52:53], 0 op_sel_hi:[1,0]
	v_pk_add_f32 v[52:53], v[44:45], 0 op_sel_hi:[1,0]
	v_pk_add_f32 v[44:45], v[42:43], 0 op_sel_hi:[1,0]
	v_cvt_pk_bf16_f32 v42, v50, v51
	v_cvt_pk_bf16_f32 v43, v48, v49
	v_add_co_u32_e32 v48, vcc, s62, v142
	v_cvt_pk_bf16_f32 v44, v44, v45
	v_cvt_pk_bf16_f32 v45, v52, v53
	v_lshl_add_u64 v[46:47], v[142:143], 0, s[14:15]
	s_nop 0
	v_addc_co_u32_e32 v49, vcc, 0, v143, vcc
	global_store_dwordx4 v[48:49], v[42:45], off sc1
	s_nop 1
	v_pk_add_f32 v[42:43], v[32:33], 0 op_sel_hi:[1,0]
	v_pk_add_f32 v[32:33], v[30:31], 0 op_sel_hi:[1,0]
	v_cvt_pk_bf16_f32 v30, v38, v39
	v_cvt_pk_bf16_f32 v31, v40, v41
	s_nop 0
	v_cvt_pk_bf16_f32 v32, v32, v33
	v_cvt_pk_bf16_f32 v33, v42, v43
	global_store_dwordx4 v[46:47], v[30:33], off offset:256 sc1
	s_nop 1
	v_pk_add_f32 v[32:33], v[36:37], 0 op_sel_hi:[1,0]
	v_pk_add_f32 v[36:37], v[28:29], 0 op_sel_hi:[1,0]
	v_pk_add_f32 v[28:29], v[26:27], 0 op_sel_hi:[1,0]
	v_cvt_pk_bf16_f32 v26, v34, v35
	v_cvt_pk_bf16_f32 v27, v32, v33
	v_add_co_u32_e32 v32, vcc, s63, v142
	v_cvt_pk_bf16_f32 v28, v28, v29
	v_cvt_pk_bf16_f32 v29, v36, v37
	v_lshl_add_u64 v[30:31], v[142:143], 0, s[16:17]
	s_nop 0
	v_addc_co_u32_e32 v33, vcc, 0, v143, vcc
	global_store_dwordx4 v[32:33], v[26:29], off sc1
	s_nop 1
	v_pk_add_f32 v[26:27], v[16:17], 0 op_sel_hi:[1,0]
	v_pk_add_f32 v[16:17], v[14:15], 0 op_sel_hi:[1,0]
	v_cvt_pk_bf16_f32 v14, v22, v23
	v_cvt_pk_bf16_f32 v15, v24, v25
	s_nop 0
	v_cvt_pk_bf16_f32 v16, v16, v17
	v_cvt_pk_bf16_f32 v17, v26, v27
	global_store_dwordx4 v[30:31], v[14:17], off offset:256 sc1
	s_nop 1
	v_pk_add_f32 v[16:17], v[20:21], 0 op_sel_hi:[1,0]
	v_pk_add_f32 v[20:21], v[12:13], 0 op_sel_hi:[1,0]
	v_pk_add_f32 v[12:13], v[10:11], 0 op_sel_hi:[1,0]
	v_cvt_pk_bf16_f32 v10, v18, v19
	v_cvt_pk_bf16_f32 v11, v16, v17
	v_add_co_u32_e32 v16, vcc, s64, v142
	v_lshl_add_u64 v[14:15], v[142:143], 0, s[18:19]
	s_nop 0
	v_addc_co_u32_e32 v17, vcc, 0, v143, vcc
	v_cvt_pk_bf16_f32 v12, v12, v13
	v_cvt_pk_bf16_f32 v13, v20, v21
	global_store_dwordx4 v[16:17], v[10:13], off sc1
	s_andn2_b64 vcc, exec, s[20:21]
	s_mov_b64 s[20:21], -1
	v_pk_add_f32 v[10:11], v[4:5], 0 op_sel_hi:[1,0]
	v_pk_add_f32 v[4:5], v[2:3], 0 op_sel_hi:[1,0]
	v_cvt_pk_bf16_f32 v2, v6, v7
	v_cvt_pk_bf16_f32 v3, v8, v9
	s_nop 0
	v_cvt_pk_bf16_f32 v4, v4, v5
	v_cvt_pk_bf16_f32 v5, v10, v11
	global_store_dwordx4 v[14:15], v[2:5], off offset:256 sc1
	s_cbranch_vccnz .LBB0_556
	s_andn2_b64 vcc, exec, s[2:3]
	s_cbranch_vccnz .LBB0_555
	s_barrier
	s_branch .LBB0_555

.LBB0_591:
	v_lshl_add_u32 v144, s28, 8, v146
	v_lshl_or_b32 v142, s61, 8, v148
	v_ashrrev_i32_e32 v143, 31, v142
	v_ashrrev_i32_e32 v145, 31, v144
	v_lshl_add_u64 v[152:153], v[142:143], 1, s[0:1]
	v_lshlrev_b64 v[142:143], 11, v[144:145]
	v_lshl_add_u64 v[142:143], v[152:153], 0, v[142:143]
	v_pk_add_f32 v[128:129], v[128:129], 0 op_sel_hi:[1,0]
	v_pk_add_f32 v[126:127], v[126:127], 0 op_sel_hi:[1,0]
	v_pk_add_f32 v[154:155], v[124:125], 0 op_sel_hi:[1,0]
	v_pk_add_f32 v[124:125], v[122:123], 0 op_sel_hi:[1,0]
	v_cvt_pk_bf16_f32 v122, v126, v127
	v_cvt_pk_bf16_f32 v123, v128, v129
	v_pk_add_f32 v[118:119], v[118:119], 0 op_sel_hi:[1,0]
	v_cvt_pk_bf16_f32 v124, v124, v125
	v_cvt_pk_bf16_f32 v125, v154, v155
	global_store_dwordx4 v[142:143], v[122:125], off sc1
	v_pk_add_f32 v[120:121], v[120:121], 0 op_sel_hi:[1,0]
	v_pk_add_f32 v[114:115], v[114:115], 0 op_sel_hi:[1,0]
	v_pk_add_f32 v[122:123], v[112:113], 0 op_sel_hi:[1,0]
	v_pk_add_f32 v[112:113], v[110:111], 0 op_sel_hi:[1,0]
	v_cvt_pk_bf16_f32 v110, v118, v119
	v_cvt_pk_bf16_f32 v111, v120, v121
	v_pk_add_f32 v[102:103], v[102:103], 0 op_sel_hi:[1,0]
	v_cvt_pk_bf16_f32 v112, v112, v113
	v_cvt_pk_bf16_f32 v113, v122, v123
	global_store_dwordx4 v[142:143], v[110:113], off offset:256 sc1
	v_pk_add_f32 v[104:105], v[104:105], 0 op_sel_hi:[1,0]
	v_pk_add_f32 v[98:99], v[98:99], 0 op_sel_hi:[1,0]
	v_or_b32_e32 v110, 16, v144
	v_ashrrev_i32_e32 v111, 31, v110
	v_lshlrev_b64 v[110:111], 11, v[110:111]
	v_lshl_add_u64 v[110:111], v[152:153], 0, v[110:111]
	v_pk_add_f32 v[112:113], v[116:117], 0 op_sel_hi:[1,0]
	v_pk_add_f32 v[116:117], v[108:109], 0 op_sel_hi:[1,0]
	v_pk_add_f32 v[108:109], v[106:107], 0 op_sel_hi:[1,0]
	v_cvt_pk_bf16_f32 v106, v114, v115
	v_cvt_pk_bf16_f32 v107, v112, v113
	v_pk_add_f32 v[86:87], v[86:87], 0 op_sel_hi:[1,0]
	v_cvt_pk_bf16_f32 v108, v108, v109
	v_cvt_pk_bf16_f32 v109, v116, v117
	global_store_dwordx4 v[110:111], v[106:109], off sc1
	v_pk_add_f32 v[88:89], v[88:89], 0 op_sel_hi:[1,0]
	v_pk_add_f32 v[82:83], v[82:83], 0 op_sel_hi:[1,0]
	v_pk_add_f32 v[106:107], v[96:97], 0 op_sel_hi:[1,0]
	v_pk_add_f32 v[96:97], v[94:95], 0 op_sel_hi:[1,0]
	v_cvt_pk_bf16_f32 v94, v102, v103
	v_cvt_pk_bf16_f32 v95, v104, v105
	v_pk_add_f32 v[72:73], v[72:73], 0 op_sel_hi:[1,0]
	v_cvt_pk_bf16_f32 v96, v96, v97
	v_cvt_pk_bf16_f32 v97, v106, v107
	global_store_dwordx4 v[110:111], v[94:97], off offset:256 sc1
	v_pk_add_f32 v[70:71], v[70:71], 0 op_sel_hi:[1,0]
	v_pk_add_f32 v[62:63], v[62:63], 0 op_sel_hi:[1,0]
	v_or_b32_e32 v94, 32, v144
	v_ashrrev_i32_e32 v95, 31, v94
	v_lshlrev_b64 v[94:95], 11, v[94:95]
	v_lshl_add_u64 v[94:95], v[152:153], 0, v[94:95]
	v_pk_add_f32 v[96:97], v[100:101], 0 op_sel_hi:[1,0]
	v_pk_add_f32 v[100:101], v[92:93], 0 op_sel_hi:[1,0]
	v_pk_add_f32 v[92:93], v[90:91], 0 op_sel_hi:[1,0]
	v_cvt_pk_bf16_f32 v90, v98, v99
	v_cvt_pk_bf16_f32 v91, v96, v97
	v_pk_add_f32 v[64:65], v[64:65], 0 op_sel_hi:[1,0]
	v_cvt_pk_bf16_f32 v92, v92, v93
	v_cvt_pk_bf16_f32 v93, v100, v101
	global_store_dwordx4 v[94:95], v[90:93], off sc1
	v_pk_add_f32 v[56:57], v[56:57], 0 op_sel_hi:[1,0]
	v_pk_add_f32 v[54:55], v[54:55], 0 op_sel_hi:[1,0]
	v_pk_add_f32 v[90:91], v[80:81], 0 op_sel_hi:[1,0]
	v_pk_add_f32 v[80:81], v[78:79], 0 op_sel_hi:[1,0]
	v_cvt_pk_bf16_f32 v78, v86, v87
	v_cvt_pk_bf16_f32 v79, v88, v89
	v_pk_add_f32 v[50:51], v[50:51], 0 op_sel_hi:[1,0]
	v_cvt_pk_bf16_f32 v80, v80, v81
	v_cvt_pk_bf16_f32 v81, v90, v91
	global_store_dwordx4 v[94:95], v[78:81], off offset:256 sc1
	v_pk_add_f32 v[40:41], v[40:41], 0 op_sel_hi:[1,0]
	v_pk_add_f32 v[38:39], v[38:39], 0 op_sel_hi:[1,0]
	v_or_b32_e32 v78, 48, v144
	v_ashrrev_i32_e32 v79, 31, v78
	v_lshlrev_b64 v[78:79], 11, v[78:79]
	v_lshl_add_u64 v[78:79], v[152:153], 0, v[78:79]
	v_pk_add_f32 v[80:81], v[84:85], 0 op_sel_hi:[1,0]
	v_pk_add_f32 v[84:85], v[76:77], 0 op_sel_hi:[1,0]
	v_pk_add_f32 v[76:77], v[74:75], 0 op_sel_hi:[1,0]
	v_cvt_pk_bf16_f32 v74, v82, v83
	v_cvt_pk_bf16_f32 v75, v80, v81
	v_pk_add_f32 v[34:35], v[34:35], 0 op_sel_hi:[1,0]
	v_cvt_pk_bf16_f32 v76, v76, v77
	v_cvt_pk_bf16_f32 v77, v84, v85
	global_store_dwordx4 v[78:79], v[74:77], off sc1
	v_pk_add_f32 v[24:25], v[24:25], 0 op_sel_hi:[1,0]
	v_pk_add_f32 v[22:23], v[22:23], 0 op_sel_hi:[1,0]
	v_pk_add_f32 v[74:75], v[68:69], 0 op_sel_hi:[1,0]
	v_pk_add_f32 v[68:69], v[66:67], 0 op_sel_hi:[1,0]
	v_cvt_pk_bf16_f32 v66, v70, v71
	v_cvt_pk_bf16_f32 v67, v72, v73
	v_pk_add_f32 v[18:19], v[18:19], 0 op_sel_hi:[1,0]
	v_cvt_pk_bf16_f32 v68, v68, v69
	v_cvt_pk_bf16_f32 v69, v74, v75
	global_store_dwordx4 v[78:79], v[66:69], off offset:256 sc1
	v_pk_add_f32 v[8:9], v[8:9], 0 op_sel_hi:[1,0]
	v_pk_add_f32 v[6:7], v[6:7], 0 op_sel_hi:[1,0]
	v_pk_add_f32 v[68:69], v[60:61], 0 op_sel_hi:[1,0]
	v_pk_add_f32 v[60:61], v[58:59], 0 op_sel_hi:[1,0]
	v_cvt_pk_bf16_f32 v58, v62, v63
	v_add_co_u32_e32 v62, vcc, s56, v142
	v_cvt_pk_bf16_f32 v59, v64, v65
	v_cvt_pk_bf16_f32 v60, v60, v61
	v_cvt_pk_bf16_f32 v61, v68, v69
	v_lshl_add_u64 v[66:67], v[142:143], 0, s[10:11]
	s_nop 0
	v_addc_co_u32_e32 v63, vcc, 0, v143, vcc
	global_store_dwordx4 v[62:63], v[58:61], off sc1
	s_nop 1
	v_pk_add_f32 v[58:59], v[48:49], 0 op_sel_hi:[1,0]
	v_pk_add_f32 v[48:49], v[46:47], 0 op_sel_hi:[1,0]
	v_cvt_pk_bf16_f32 v46, v54, v55
	v_cvt_pk_bf16_f32 v47, v56, v57
	s_nop 0
	v_cvt_pk_bf16_f32 v48, v48, v49
	v_cvt_pk_bf16_f32 v49, v58, v59
	global_store_dwordx4 v[66:67], v[46:49], off offset:256 sc1
	s_nop 1
	v_pk_add_f32 v[48:49], v[52:53], 0 op_sel_hi:[1,0]
	v_pk_add_f32 v[52:53], v[44:45], 0 op_sel_hi:[1,0]
	v_pk_add_f32 v[44:45], v[42:43], 0 op_sel_hi:[1,0]
	v_cvt_pk_bf16_f32 v42, v50, v51
	v_cvt_pk_bf16_f32 v43, v48, v49
	v_add_co_u32_e32 v48, vcc, s57, v142
	v_cvt_pk_bf16_f32 v44, v44, v45
	v_cvt_pk_bf16_f32 v45, v52, v53
	v_lshl_add_u64 v[46:47], v[142:143], 0, s[12:13]
	s_nop 0
	v_addc_co_u32_e32 v49, vcc, 0, v143, vcc
	global_store_dwordx4 v[48:49], v[42:45], off sc1
	s_nop 1
	v_pk_add_f32 v[42:43], v[32:33], 0 op_sel_hi:[1,0]
	v_pk_add_f32 v[32:33], v[30:31], 0 op_sel_hi:[1,0]
	v_cvt_pk_bf16_f32 v30, v38, v39
	v_cvt_pk_bf16_f32 v31, v40, v41
	s_nop 0
	v_cvt_pk_bf16_f32 v32, v32, v33
	v_cvt_pk_bf16_f32 v33, v42, v43
	global_store_dwordx4 v[46:47], v[30:33], off offset:256 sc1
	s_nop 1
	v_pk_add_f32 v[32:33], v[36:37], 0 op_sel_hi:[1,0]
	v_pk_add_f32 v[36:37], v[28:29], 0 op_sel_hi:[1,0]
	v_pk_add_f32 v[28:29], v[26:27], 0 op_sel_hi:[1,0]
	v_cvt_pk_bf16_f32 v26, v34, v35
	v_cvt_pk_bf16_f32 v27, v32, v33
	v_add_co_u32_e32 v32, vcc, s58, v142
	v_cvt_pk_bf16_f32 v28, v28, v29
	v_cvt_pk_bf16_f32 v29, v36, v37
	v_lshl_add_u64 v[30:31], v[142:143], 0, s[14:15]
	s_nop 0
	v_addc_co_u32_e32 v33, vcc, 0, v143, vcc
	global_store_dwordx4 v[32:33], v[26:29], off sc1
	s_nop 1
	v_pk_add_f32 v[26:27], v[16:17], 0 op_sel_hi:[1,0]
	v_pk_add_f32 v[16:17], v[14:15], 0 op_sel_hi:[1,0]
	v_cvt_pk_bf16_f32 v14, v22, v23
	v_cvt_pk_bf16_f32 v15, v24, v25
	s_nop 0
	v_cvt_pk_bf16_f32 v16, v16, v17
	v_cvt_pk_bf16_f32 v17, v26, v27
	global_store_dwordx4 v[30:31], v[14:17], off offset:256 sc1
	s_nop 1
	v_pk_add_f32 v[16:17], v[20:21], 0 op_sel_hi:[1,0]
	v_pk_add_f32 v[20:21], v[12:13], 0 op_sel_hi:[1,0]
	v_pk_add_f32 v[12:13], v[10:11], 0 op_sel_hi:[1,0]
	v_cvt_pk_bf16_f32 v10, v18, v19
	v_cvt_pk_bf16_f32 v11, v16, v17
	v_add_co_u32_e32 v16, vcc, s59, v142
	v_lshl_add_u64 v[14:15], v[142:143], 0, s[16:17]
	s_nop 0
	v_addc_co_u32_e32 v17, vcc, 0, v143, vcc
	v_cvt_pk_bf16_f32 v12, v12, v13
	v_cvt_pk_bf16_f32 v13, v20, v21
	global_store_dwordx4 v[16:17], v[10:13], off sc1
	s_andn2_b64 vcc, exec, s[18:19]
	s_mov_b64 s[18:19], -1
	v_pk_add_f32 v[10:11], v[4:5], 0 op_sel_hi:[1,0]
	v_pk_add_f32 v[4:5], v[2:3], 0 op_sel_hi:[1,0]
	v_cvt_pk_bf16_f32 v2, v6, v7
	v_cvt_pk_bf16_f32 v3, v8, v9
	s_nop 0
	v_cvt_pk_bf16_f32 v4, v4, v5
	v_cvt_pk_bf16_f32 v5, v10, v11
	global_store_dwordx4 v[14:15], v[2:5], off offset:256 sc1
	s_cbranch_vccnz .LBB0_580
	s_andn2_b64 vcc, exec, s[2:3]
	s_cbranch_vccnz .LBB0_579
	s_barrier
	s_branch .LBB0_579

.LBB0_727:
	v_lshl_add_u32 v148, s28, 8, v150
	v_lshl_or_b32 v146, s55, 8, v152
	v_ashrrev_i32_e32 v149, 31, v148
	v_ashrrev_i32_e32 v147, 31, v146
	v_lshlrev_b64 v[144:145], 12, v[148:149]
	v_lshl_add_u64 v[144:145], v[144:145], 0, v[146:147]
	v_lshlrev_b64 v[144:145], 1, v[144:145]
	v_lshl_add_u64 v[160:161], s[2:3], 0, v[144:145]
	global_load_dwordx4 v[156:159], v[160:161], off
	s_andn2_b64 vcc, exec, s[4:5]
	s_mov_b64 s[4:5], -1
	s_waitcnt vmcnt(0)
	v_lshlrev_b32_e32 v149, 16, v156
	v_and_b32_e32 v156, 0xffff0000, v156
	v_lshlrev_b32_e32 v162, 16, v157
	v_and_b32_e32 v157, 0xffff0000, v157
	v_lshlrev_b32_e32 v164, 16, v159
	v_and_b32_e32 v159, 0xffff0000, v159
	v_lshlrev_b32_e32 v163, 16, v158
	v_and_b32_e32 v158, 0xffff0000, v158
	v_add_f32_e32 v124, v124, v149
	v_add_f32_e32 v125, v125, v156
	v_add_f32_e32 v126, v126, v162
	v_add_f32_e32 v127, v127, v157
	v_add_f32_e32 v123, v123, v159
	v_add_f32_e32 v149, v120, v163
	v_add_f32_e32 v156, v121, v158
	v_add_f32_e32 v157, v122, v164
	v_cvt_pk_bf16_f32 v120, v124, v125
	v_cvt_pk_bf16_f32 v121, v126, v127
	v_cvt_pk_bf16_f32 v122, v149, v156
	v_cvt_pk_bf16_f32 v123, v157, v123
	global_load_dwordx4 v[124:127], v[160:161], off offset:256
	v_or_b32_e32 v156, 16, v148
	v_ashrrev_i32_e32 v157, 31, v156
	v_lshlrev_b64 v[156:157], 12, v[156:157]
	v_lshl_add_u64 v[158:159], s[6:7], 0, v[144:145]
	v_lshl_add_u64 v[156:157], v[156:157], 0, v[146:147]
	global_store_dwordx4 v[158:159], v[120:123], off sc1
	v_lshlrev_b64 v[156:157], 1, v[156:157]
	v_lshl_add_u64 v[160:161], s[2:3], 0, v[156:157]
	s_waitcnt vmcnt(1)
	v_lshlrev_b32_e32 v120, 16, v124
	v_and_b32_e32 v121, 0xffff0000, v124
	v_lshlrev_b32_e32 v122, 16, v125
	v_and_b32_e32 v123, 0xffff0000, v125
	v_lshlrev_b32_e32 v124, 16, v126
	v_and_b32_e32 v125, 0xffff0000, v126
	v_lshlrev_b32_e32 v126, 16, v127
	v_and_b32_e32 v127, 0xffff0000, v127
	v_add_f32_e32 v111, v111, v127
	v_add_f32_e32 v116, v116, v120
	v_add_f32_e32 v117, v117, v121
	v_add_f32_e32 v118, v118, v122
	v_add_f32_e32 v119, v119, v123
	v_add_f32_e32 v120, v108, v124
	v_add_f32_e32 v121, v109, v125
	v_add_f32_e32 v122, v110, v126
	v_cvt_pk_bf16_f32 v108, v116, v117
	v_cvt_pk_bf16_f32 v109, v118, v119
	v_cvt_pk_bf16_f32 v110, v120, v121
	v_cvt_pk_bf16_f32 v111, v122, v111
	global_store_dwordx4 v[158:159], v[108:111], off offset:256 sc1
	global_load_dwordx4 v[108:111], v[160:161], off
	s_waitcnt vmcnt(0)
	v_lshlrev_b32_e32 v116, 16, v108
	v_and_b32_e32 v108, 0xffff0000, v108
	v_lshlrev_b32_e32 v117, 16, v109
	v_and_b32_e32 v109, 0xffff0000, v109
	v_lshlrev_b32_e32 v118, 16, v110
	v_and_b32_e32 v110, 0xffff0000, v110
	v_lshlrev_b32_e32 v119, 16, v111
	v_and_b32_e32 v111, 0xffff0000, v111
	v_add_f32_e32 v108, v113, v108
	v_add_f32_e32 v109, v115, v109
	v_add_f32_e32 v110, v105, v110
	v_add_f32_e32 v107, v107, v111
	v_add_f32_e32 v112, v112, v116
	v_add_f32_e32 v113, v114, v117
	v_add_f32_e32 v114, v104, v118
	v_add_f32_e32 v115, v106, v119
	v_cvt_pk_bf16_f32 v104, v112, v108
	v_cvt_pk_bf16_f32 v105, v113, v109
	v_cvt_pk_bf16_f32 v106, v114, v110
	v_cvt_pk_bf16_f32 v107, v115, v107
	global_load_dwordx4 v[108:111], v[160:161], off offset:256
	v_or_b32_e32 v112, 32, v148
	v_ashrrev_i32_e32 v113, 31, v112
	v_lshlrev_b64 v[112:113], 12, v[112:113]
	v_lshl_add_u64 v[114:115], s[6:7], 0, v[156:157]
	v_lshl_add_u64 v[112:113], v[112:113], 0, v[146:147]
	global_store_dwordx4 v[114:115], v[104:107], off sc1
	v_lshlrev_b64 v[112:113], 1, v[112:113]
	v_lshl_add_u64 v[116:117], s[2:3], 0, v[112:113]
	s_waitcnt vmcnt(1)
	v_lshlrev_b32_e32 v104, 16, v108
	v_and_b32_e32 v105, 0xffff0000, v108
	v_lshlrev_b32_e32 v106, 16, v109
	v_and_b32_e32 v107, 0xffff0000, v109
	v_lshlrev_b32_e32 v108, 16, v110
	v_and_b32_e32 v109, 0xffff0000, v110
	v_lshlrev_b32_e32 v110, 16, v111
	v_and_b32_e32 v111, 0xffff0000, v111
	v_add_f32_e32 v95, v95, v111
	v_add_f32_e32 v100, v100, v104
	v_add_f32_e32 v101, v101, v105
	v_add_f32_e32 v102, v102, v106
	v_add_f32_e32 v103, v103, v107
	v_add_f32_e32 v104, v92, v108
	v_add_f32_e32 v105, v93, v109
	v_add_f32_e32 v106, v94, v110
	v_cvt_pk_bf16_f32 v92, v100, v101
	v_cvt_pk_bf16_f32 v93, v102, v103
	v_cvt_pk_bf16_f32 v94, v104, v105
	v_cvt_pk_bf16_f32 v95, v106, v95
	global_store_dwordx4 v[114:115], v[92:95], off offset:256 sc1
	global_load_dwordx4 v[92:95], v[116:117], off
	s_waitcnt vmcnt(0)
	v_lshlrev_b32_e32 v100, 16, v92
	v_and_b32_e32 v92, 0xffff0000, v92
	v_lshlrev_b32_e32 v101, 16, v93
	v_and_b32_e32 v93, 0xffff0000, v93
	v_lshlrev_b32_e32 v102, 16, v94
	v_and_b32_e32 v94, 0xffff0000, v94
	v_lshlrev_b32_e32 v103, 16, v95
	v_and_b32_e32 v95, 0xffff0000, v95
	v_add_f32_e32 v92, v97, v92
	v_add_f32_e32 v93, v99, v93
	v_add_f32_e32 v94, v89, v94
	v_add_f32_e32 v91, v91, v95
	v_add_f32_e32 v96, v96, v100
	v_add_f32_e32 v97, v98, v101
	v_add_f32_e32 v98, v88, v102
	v_add_f32_e32 v99, v90, v103
	v_cvt_pk_bf16_f32 v88, v96, v92
	v_cvt_pk_bf16_f32 v89, v97, v93
	v_cvt_pk_bf16_f32 v90, v98, v94
	v_cvt_pk_bf16_f32 v91, v99, v91
	global_load_dwordx4 v[92:95], v[116:117], off offset:256
	v_or_b32_e32 v96, 48, v148
	v_ashrrev_i32_e32 v97, 31, v96
	v_lshlrev_b64 v[96:97], 12, v[96:97]
	v_lshl_add_u64 v[98:99], s[6:7], 0, v[112:113]
	v_lshl_add_u64 v[96:97], v[96:97], 0, v[146:147]
	global_store_dwordx4 v[98:99], v[88:91], off sc1
	v_lshlrev_b64 v[96:97], 1, v[96:97]
	v_lshl_add_u64 v[100:101], s[2:3], 0, v[96:97]
	s_waitcnt vmcnt(1)
	v_lshlrev_b32_e32 v88, 16, v92
	v_and_b32_e32 v89, 0xffff0000, v92
	v_lshlrev_b32_e32 v90, 16, v93
	v_and_b32_e32 v91, 0xffff0000, v93
	v_lshlrev_b32_e32 v92, 16, v94
	v_and_b32_e32 v93, 0xffff0000, v94
	v_lshlrev_b32_e32 v94, 16, v95
	v_and_b32_e32 v95, 0xffff0000, v95
	v_add_f32_e32 v79, v79, v95
	v_add_f32_e32 v84, v84, v88
	v_add_f32_e32 v85, v85, v89
	v_add_f32_e32 v86, v86, v90
	v_add_f32_e32 v87, v87, v91
	v_add_f32_e32 v88, v76, v92
	v_add_f32_e32 v89, v77, v93
	v_add_f32_e32 v90, v78, v94
	v_cvt_pk_bf16_f32 v76, v84, v85
	v_cvt_pk_bf16_f32 v77, v86, v87
	v_cvt_pk_bf16_f32 v78, v88, v89
	v_cvt_pk_bf16_f32 v79, v90, v79
	global_store_dwordx4 v[98:99], v[76:79], off offset:256 sc1
	global_load_dwordx4 v[76:79], v[100:101], off
	s_waitcnt vmcnt(0)
	v_lshlrev_b32_e32 v84, 16, v76
	v_and_b32_e32 v76, 0xffff0000, v76
	v_lshlrev_b32_e32 v85, 16, v77
	v_and_b32_e32 v77, 0xffff0000, v77
	v_lshlrev_b32_e32 v86, 16, v78
	v_and_b32_e32 v78, 0xffff0000, v78
	v_lshlrev_b32_e32 v87, 16, v79
	v_and_b32_e32 v79, 0xffff0000, v79
	v_add_f32_e32 v76, v81, v76
	v_add_f32_e32 v77, v83, v77
	v_add_f32_e32 v78, v73, v78
	v_add_f32_e32 v75, v75, v79
	v_add_f32_e32 v80, v80, v84
	v_add_f32_e32 v81, v82, v85
	v_add_f32_e32 v82, v72, v86
	v_add_f32_e32 v83, v74, v87
	v_cvt_pk_bf16_f32 v72, v80, v76
	v_cvt_pk_bf16_f32 v73, v81, v77
	v_cvt_pk_bf16_f32 v74, v82, v78
	v_cvt_pk_bf16_f32 v75, v83, v75
	global_load_dwordx4 v[76:79], v[100:101], off offset:256
	v_lshl_add_u64 v[82:83], s[6:7], 0, v[96:97]
	global_store_dwordx4 v[82:83], v[72:75], off sc1
	v_lshl_add_u64 v[80:81], v[144:145], 0, s[12:13]
	v_lshl_add_u64 v[84:85], s[2:3], 0, v[80:81]
	s_waitcnt vmcnt(1)
	v_lshlrev_b32_e32 v72, 16, v76
	v_and_b32_e32 v73, 0xffff0000, v76
	v_lshlrev_b32_e32 v74, 16, v77
	v_and_b32_e32 v75, 0xffff0000, v77
	v_lshlrev_b32_e32 v76, 16, v78
	v_and_b32_e32 v77, 0xffff0000, v78
	v_lshlrev_b32_e32 v78, 16, v79
	v_and_b32_e32 v79, 0xffff0000, v79
	v_add_f32_e32 v67, v67, v79
	v_add_f32_e32 v68, v68, v72
	v_add_f32_e32 v69, v69, v73
	v_add_f32_e32 v70, v70, v74
	v_add_f32_e32 v71, v71, v75
	v_add_f32_e32 v72, v64, v76
	v_add_f32_e32 v73, v65, v77
	v_add_f32_e32 v74, v66, v78
	v_cvt_pk_bf16_f32 v64, v68, v69
	v_cvt_pk_bf16_f32 v65, v70, v71
	v_cvt_pk_bf16_f32 v66, v72, v73
	v_cvt_pk_bf16_f32 v67, v74, v67
	global_store_dwordx4 v[82:83], v[64:67], off offset:256 sc1
	global_load_dwordx4 v[64:67], v[84:85], off
	s_waitcnt vmcnt(0)
	v_lshlrev_b32_e32 v68, 16, v64
	v_and_b32_e32 v64, 0xffff0000, v64
	v_lshlrev_b32_e32 v69, 16, v65
	v_and_b32_e32 v65, 0xffff0000, v65
	v_lshlrev_b32_e32 v71, 16, v67
	v_and_b32_e32 v67, 0xffff0000, v67
	v_lshlrev_b32_e32 v70, 16, v66
	v_and_b32_e32 v66, 0xffff0000, v66
	v_add_f32_e32 v60, v60, v68
	v_add_f32_e32 v61, v61, v64
	v_add_f32_e32 v62, v62, v69
	v_add_f32_e32 v63, v63, v65
	v_add_f32_e32 v59, v59, v67
	v_add_f32_e32 v64, v56, v70
	v_add_f32_e32 v65, v57, v66
	v_add_f32_e32 v66, v58, v71
	v_cvt_pk_bf16_f32 v56, v60, v61
	v_cvt_pk_bf16_f32 v57, v62, v63
	v_cvt_pk_bf16_f32 v58, v64, v65
	v_cvt_pk_bf16_f32 v59, v66, v59
	global_load_dwordx4 v[60:63], v[84:85], off offset:256
	v_lshl_add_u64 v[66:67], s[6:7], 0, v[80:81]
	global_store_dwordx4 v[66:67], v[56:59], off sc1
	v_lshl_add_u64 v[64:65], v[144:145], 0, s[14:15]
	v_lshl_add_u64 v[68:69], s[2:3], 0, v[64:65]
	s_waitcnt vmcnt(1)
	v_lshlrev_b32_e32 v56, 16, v60
	v_and_b32_e32 v57, 0xffff0000, v60
	v_lshlrev_b32_e32 v58, 16, v61
	v_and_b32_e32 v59, 0xffff0000, v61
	v_lshlrev_b32_e32 v60, 16, v62
	v_and_b32_e32 v61, 0xffff0000, v62
	v_lshlrev_b32_e32 v62, 16, v63
	v_and_b32_e32 v63, 0xffff0000, v63
	v_add_f32_e32 v47, v47, v63
	v_add_f32_e32 v52, v52, v56
	v_add_f32_e32 v53, v53, v57
	v_add_f32_e32 v54, v54, v58
	v_add_f32_e32 v55, v55, v59
	v_add_f32_e32 v56, v44, v60
	v_add_f32_e32 v57, v45, v61
	v_add_f32_e32 v58, v46, v62
	v_cvt_pk_bf16_f32 v44, v52, v53
	v_cvt_pk_bf16_f32 v45, v54, v55
	v_cvt_pk_bf16_f32 v46, v56, v57
	v_cvt_pk_bf16_f32 v47, v58, v47
	global_store_dwordx4 v[66:67], v[44:47], off offset:256 sc1
	global_load_dwordx4 v[44:47], v[68:69], off
	s_waitcnt vmcnt(0)
	v_lshlrev_b32_e32 v52, 16, v44
	v_and_b32_e32 v44, 0xffff0000, v44
	v_lshlrev_b32_e32 v53, 16, v45
	v_and_b32_e32 v45, 0xffff0000, v45
	v_lshlrev_b32_e32 v54, 16, v46
	v_and_b32_e32 v46, 0xffff0000, v46
	v_lshlrev_b32_e32 v55, 16, v47
	v_and_b32_e32 v47, 0xffff0000, v47
	v_add_f32_e32 v44, v49, v44
	v_add_f32_e32 v45, v51, v45
	v_add_f32_e32 v46, v41, v46
	v_add_f32_e32 v43, v43, v47
	v_add_f32_e32 v48, v48, v52
	v_add_f32_e32 v49, v50, v53
	v_add_f32_e32 v50, v40, v54
	v_add_f32_e32 v51, v42, v55
	v_cvt_pk_bf16_f32 v40, v48, v44
	v_cvt_pk_bf16_f32 v41, v49, v45
	v_cvt_pk_bf16_f32 v42, v50, v46
	v_cvt_pk_bf16_f32 v43, v51, v43
	global_load_dwordx4 v[44:47], v[68:69], off offset:256
	v_lshl_add_u64 v[50:51], s[6:7], 0, v[64:65]
	global_store_dwordx4 v[50:51], v[40:43], off sc1
	v_lshl_add_u64 v[48:49], v[144:145], 0, s[16:17]
	v_lshl_add_u64 v[52:53], s[2:3], 0, v[48:49]
	s_waitcnt vmcnt(1)
	v_lshlrev_b32_e32 v40, 16, v44
	v_and_b32_e32 v41, 0xffff0000, v44
	v_lshlrev_b32_e32 v42, 16, v45
	v_and_b32_e32 v43, 0xffff0000, v45
	v_lshlrev_b32_e32 v44, 16, v46
	v_and_b32_e32 v45, 0xffff0000, v46
	v_lshlrev_b32_e32 v46, 16, v47
	v_and_b32_e32 v47, 0xffff0000, v47
	v_add_f32_e32 v31, v31, v47
	v_add_f32_e32 v36, v36, v40
	v_add_f32_e32 v37, v37, v41
	v_add_f32_e32 v38, v38, v42
	v_add_f32_e32 v39, v39, v43
	v_add_f32_e32 v40, v28, v44
	v_add_f32_e32 v41, v29, v45
	v_add_f32_e32 v42, v30, v46
	v_cvt_pk_bf16_f32 v28, v36, v37
	v_cvt_pk_bf16_f32 v29, v38, v39
	v_cvt_pk_bf16_f32 v30, v40, v41
	v_cvt_pk_bf16_f32 v31, v42, v31
	global_store_dwordx4 v[50:51], v[28:31], off offset:256 sc1
	global_load_dwordx4 v[28:31], v[52:53], off
	s_waitcnt vmcnt(0)
	v_lshlrev_b32_e32 v36, 16, v28
	v_and_b32_e32 v28, 0xffff0000, v28
	v_lshlrev_b32_e32 v37, 16, v29
	v_and_b32_e32 v29, 0xffff0000, v29
	v_lshlrev_b32_e32 v38, 16, v30
	v_and_b32_e32 v30, 0xffff0000, v30
	v_lshlrev_b32_e32 v39, 16, v31
	v_and_b32_e32 v31, 0xffff0000, v31
	v_add_f32_e32 v28, v33, v28
	v_add_f32_e32 v29, v35, v29
	v_add_f32_e32 v30, v25, v30
	v_add_f32_e32 v27, v27, v31
	v_add_f32_e32 v32, v32, v36
	v_add_f32_e32 v33, v34, v37
	v_add_f32_e32 v34, v24, v38
	v_add_f32_e32 v35, v26, v39
	v_cvt_pk_bf16_f32 v24, v32, v28
	v_cvt_pk_bf16_f32 v25, v33, v29
	v_cvt_pk_bf16_f32 v26, v34, v30
	v_cvt_pk_bf16_f32 v27, v35, v27
	global_load_dwordx4 v[28:31], v[52:53], off offset:256
	v_lshl_add_u64 v[34:35], s[6:7], 0, v[48:49]
	global_store_dwordx4 v[34:35], v[24:27], off sc1
	v_lshl_add_u64 v[32:33], v[144:145], 0, s[18:19]
	v_lshl_add_u64 v[36:37], s[2:3], 0, v[32:33]
	s_waitcnt vmcnt(1)
	v_lshlrev_b32_e32 v24, 16, v28
	v_and_b32_e32 v25, 0xffff0000, v28
	v_lshlrev_b32_e32 v26, 16, v29
	v_and_b32_e32 v27, 0xffff0000, v29
	v_lshlrev_b32_e32 v28, 16, v30
	v_and_b32_e32 v29, 0xffff0000, v30
	v_lshlrev_b32_e32 v30, 16, v31
	v_and_b32_e32 v31, 0xffff0000, v31
	v_add_f32_e32 v15, v15, v31
	v_add_f32_e32 v20, v20, v24
	v_add_f32_e32 v21, v21, v25
	v_add_f32_e32 v22, v22, v26
	v_add_f32_e32 v23, v23, v27
	v_add_f32_e32 v24, v12, v28
	v_add_f32_e32 v25, v13, v29
	v_add_f32_e32 v26, v14, v30
	v_cvt_pk_bf16_f32 v12, v20, v21
	v_cvt_pk_bf16_f32 v13, v22, v23
	v_cvt_pk_bf16_f32 v14, v24, v25
	v_cvt_pk_bf16_f32 v15, v26, v15
	global_store_dwordx4 v[34:35], v[12:15], off offset:256 sc1
	global_load_dwordx4 v[12:15], v[36:37], off
	s_waitcnt vmcnt(0)
	v_lshlrev_b32_e32 v20, 16, v12
	v_and_b32_e32 v12, 0xffff0000, v12
	v_lshlrev_b32_e32 v21, 16, v13
	v_and_b32_e32 v13, 0xffff0000, v13
	v_lshlrev_b32_e32 v22, 16, v14
	v_and_b32_e32 v14, 0xffff0000, v14
	v_lshlrev_b32_e32 v23, 16, v15
	v_and_b32_e32 v15, 0xffff0000, v15
	v_add_f32_e32 v12, v17, v12
	v_add_f32_e32 v13, v19, v13
	v_add_f32_e32 v14, v9, v14
	v_add_f32_e32 v11, v11, v15
	v_add_f32_e32 v16, v16, v20
	v_add_f32_e32 v17, v18, v21
	v_add_f32_e32 v18, v8, v22
	v_add_f32_e32 v19, v10, v23
	v_cvt_pk_bf16_f32 v8, v16, v12
	v_cvt_pk_bf16_f32 v9, v17, v13
	v_cvt_pk_bf16_f32 v10, v18, v14
	v_cvt_pk_bf16_f32 v11, v19, v11
	global_load_dwordx4 v[12:15], v[36:37], off offset:256
	v_lshl_add_u64 v[16:17], s[6:7], 0, v[32:33]
	global_store_dwordx4 v[16:17], v[8:11], off sc1
	s_waitcnt vmcnt(1)
	s_nop 0
	v_lshlrev_b32_e32 v8, 16, v12
	v_and_b32_e32 v9, 0xffff0000, v12
	v_lshlrev_b32_e32 v10, 16, v13
	v_and_b32_e32 v11, 0xffff0000, v13
	v_lshlrev_b32_e32 v12, 16, v14
	v_and_b32_e32 v13, 0xffff0000, v14
	v_lshlrev_b32_e32 v14, 16, v15
	v_and_b32_e32 v15, 0xffff0000, v15
	v_add_f32_e32 v3, v3, v15
	v_add_f32_e32 v4, v4, v8
	v_add_f32_e32 v5, v5, v9
	v_add_f32_e32 v6, v6, v10
	v_add_f32_e32 v7, v7, v11
	v_add_f32_e32 v8, v0, v12
	v_add_f32_e32 v9, v1, v13
	v_add_f32_e32 v10, v2, v14
	v_cvt_pk_bf16_f32 v0, v4, v5
	v_cvt_pk_bf16_f32 v1, v6, v7
	v_cvt_pk_bf16_f32 v2, v8, v9
	v_cvt_pk_bf16_f32 v3, v10, v3
	global_store_dwordx4 v[16:17], v[0:3], off offset:256 sc1
	s_cbranch_vccnz .LBB0_716
	s_andn2_b64 vcc, exec, s[0:1]
	s_cbranch_vccnz .LBB0_715
	s_barrier
	s_branch .LBB0_715
